# scan_fast trimmed: clamp instead of compare/select, packed muls, one address bump per group, peeled last 3 groups
# baseline (speedup 1.0000x reference)
.Lsc_V_setup:
	v_bfe_u32 v30, v0, 3, 4
	v_lshlrev_b32_e32 v30, 7, v30
	v_or3_b32 v2, v29, v30, v27
	v_add_u32_e32 v5, 0x8000, v24
	v_xor_b32_e32 v6, 64, v5
	v_lshlrev_b32_e32 v7, 7, v15
	v_lshl_add_u32 v7, v25, 3, v7
	s_lshl_b32 s44, s6, 11
	s_lshl_b32 s45, s7, 5
	s_add_u32 s44, s44, s45
	v_add_u32_e32 v7, s44, v7
	v_lshlrev_b32_e32 v8, 4, v25
	s_lshl_b32 s44, s7, 6
	s_add_u32 s44, s44, 0x100
	v_add_u32_e32 v8, s44, v8
	s_add_u32 s8, s30, s42
	s_addc_u32 s9, s31, 0
	s_lshl_b32 s44, s6, 11
	s_add_u32 s44, s44, s43
	s_add_u32 s10, s26, s44
	s_addc_u32 s11, s27, 0
	s_add_u32 s12, s38, s43
	s_addc_u32 s13, s39, 0
	v_add_u32_e32 v160, 0x8000, v7
	v_add_u32_e32 v161, 0x10000, v7
	v_add_u32_e32 v162, 0x18000, v7
	s_add_u32 s18, s19, 0
	s_mov_b32 m0, s18
	s_mov_b64 s[46:47], s[8:9]
	global_load_lds_dwordx4 v1, s[46:47]
	s_add_u32 m0, m0, 0x1000
	s_add_u32 s46, s46, 0x1000
	s_addc_u32 s47, s47, 0
	global_load_lds_dwordx4 v1, s[46:47]
	s_add_u32 m0, m0, 0x1000
	s_add_u32 s46, s46, 0x1000
	s_addc_u32 s47, s47, 0
	global_load_lds_dwordx4 v1, s[46:47]
	s_add_u32 m0, m0, 0x1000
	s_add_u32 s46, s46, 0x1000
	s_addc_u32 s47, s47, 0
	global_load_lds_dwordx4 v1, s[46:47]
	s_add_u32 m0, m0, 0x1000
	s_add_u32 s46, s46, 0x1000
	s_addc_u32 s47, s47, 0
	global_load_lds_dwordx4 v1, s[46:47]
	s_add_u32 m0, m0, 0x1000
	s_add_u32 s46, s46, 0x1000
	s_addc_u32 s47, s47, 0
	global_load_lds_dwordx4 v1, s[46:47]
	s_add_u32 m0, m0, 0x1000
	s_add_u32 s46, s46, 0x1000
	s_addc_u32 s47, s47, 0
	global_load_lds_dwordx4 v1, s[46:47]
	s_add_u32 m0, m0, 0x1000
	s_add_u32 s46, s46, 0x1000
	s_addc_u32 s47, s47, 0
	global_load_lds_dwordx4 v1, s[46:47]
	s_add_u32 m0, m0, 0x1000
	s_mov_b64 s[46:47], s[10:11]
	s_nop 0
	global_load_lds_dwordx4 v2, s[46:47]
	s_add_u32 m0, m0, 0x1000
	s_add_u32 s46, s46, 0x10000
	s_addc_u32 s47, s47, 0
	global_load_lds_dwordx4 v2, s[46:47]
	s_add_u32 s8, s8, 0x8000
	s_addc_u32 s9, s9, 0
	s_add_u32 s10, s10, 0x20000
	s_addc_u32 s11, s11, 0
	s_add_u32 s18, s19, 40960
	s_mov_b32 m0, s18
	s_mov_b64 s[46:47], s[8:9]
	global_load_lds_dwordx4 v1, s[46:47]
	s_add_u32 m0, m0, 0x1000
	s_add_u32 s46, s46, 0x1000
	s_addc_u32 s47, s47, 0
	global_load_lds_dwordx4 v1, s[46:47]
	s_add_u32 m0, m0, 0x1000
	s_add_u32 s46, s46, 0x1000
	s_addc_u32 s47, s47, 0
	global_load_lds_dwordx4 v1, s[46:47]
	s_add_u32 m0, m0, 0x1000
	s_add_u32 s46, s46, 0x1000
	s_addc_u32 s47, s47, 0
	global_load_lds_dwordx4 v1, s[46:47]
	s_add_u32 m0, m0, 0x1000
	s_add_u32 s46, s46, 0x1000
	s_addc_u32 s47, s47, 0
	global_load_lds_dwordx4 v1, s[46:47]
	s_add_u32 m0, m0, 0x1000
	s_add_u32 s46, s46, 0x1000
	s_addc_u32 s47, s47, 0
	global_load_lds_dwordx4 v1, s[46:47]
	s_add_u32 m0, m0, 0x1000
	s_add_u32 s46, s46, 0x1000
	s_addc_u32 s47, s47, 0
	global_load_lds_dwordx4 v1, s[46:47]
	s_add_u32 m0, m0, 0x1000
	s_add_u32 s46, s46, 0x1000
	s_addc_u32 s47, s47, 0
	global_load_lds_dwordx4 v1, s[46:47]
	s_add_u32 m0, m0, 0x1000
	s_mov_b64 s[46:47], s[10:11]
	s_nop 0
	global_load_lds_dwordx4 v2, s[46:47]
	s_add_u32 m0, m0, 0x1000
	s_add_u32 s46, s46, 0x10000
	s_addc_u32 s47, s47, 0
	global_load_lds_dwordx4 v2, s[46:47]
	s_add_u32 s8, s8, 0x8000
	s_addc_u32 s9, s9, 0
	s_add_u32 s10, s10, 0x20000
	s_addc_u32 s11, s11, 0
	s_add_u32 s18, s19, 81920
	s_mov_b32 m0, s18
	s_mov_b64 s[46:47], s[8:9]
	global_load_lds_dwordx4 v1, s[46:47]
	s_add_u32 m0, m0, 0x1000
	s_add_u32 s46, s46, 0x1000
	s_addc_u32 s47, s47, 0
	global_load_lds_dwordx4 v1, s[46:47]
	s_add_u32 m0, m0, 0x1000
	s_add_u32 s46, s46, 0x1000
	s_addc_u32 s47, s47, 0
	global_load_lds_dwordx4 v1, s[46:47]
	s_add_u32 m0, m0, 0x1000
	s_add_u32 s46, s46, 0x1000
	s_addc_u32 s47, s47, 0
	global_load_lds_dwordx4 v1, s[46:47]
	s_add_u32 m0, m0, 0x1000
	s_add_u32 s46, s46, 0x1000
	s_addc_u32 s47, s47, 0
	global_load_lds_dwordx4 v1, s[46:47]
	s_add_u32 m0, m0, 0x1000
	s_add_u32 s46, s46, 0x1000
	s_addc_u32 s47, s47, 0
	global_load_lds_dwordx4 v1, s[46:47]
	s_add_u32 m0, m0, 0x1000
	s_add_u32 s46, s46, 0x1000
	s_addc_u32 s47, s47, 0
	global_load_lds_dwordx4 v1, s[46:47]
	s_add_u32 m0, m0, 0x1000
	s_add_u32 s46, s46, 0x1000
	s_addc_u32 s47, s47, 0
	global_load_lds_dwordx4 v1, s[46:47]
	s_add_u32 m0, m0, 0x1000
	s_mov_b64 s[46:47], s[10:11]
	s_nop 0
	global_load_lds_dwordx4 v2, s[46:47]
	s_add_u32 m0, m0, 0x1000
	s_add_u32 s46, s46, 0x10000
	s_addc_u32 s47, s47, 0
	global_load_lds_dwordx4 v2, s[46:47]
	s_add_u32 s8, s8, 0x8000
	s_addc_u32 s9, s9, 0
	s_add_u32 s10, s10, 0x20000
	s_addc_u32 s11, s11, 0
	s_add_u32 s18, s19, 122880
.Lsc_V_loop:
	s_cmp_lt_u32 s16, 3
	s_cbranch_scc1 .Lsc_V_w20
	s_waitcnt vmcnt(32)
	s_branch .Lsc_V_wd

.Lsc_V_wd:
	s_barrier
	v_add_u32_e32 v140, s17, v3
	v_add_u32_e32 v141, s17, v4
	v_add_u32_e32 v142, s17, v5
	v_add_u32_e32 v143, s17, v6
	ds_read_b128 v[32:35], v140 offset:0
	ds_read_b128 v[36:39], v141 offset:0
	ds_read_b128 v[64:67], v142 offset:0
	ds_read_b128 v[68:71], v143 offset:0
	ds_read_b128 v[40:43], v140 offset:8192
	ds_read_b128 v[44:47], v141 offset:8192
	ds_read_b128 v[72:75], v142 offset:2048
	ds_read_b128 v[76:79], v143 offset:2048
	ds_read_b128 v[48:51], v140 offset:16384
	ds_read_b128 v[52:55], v141 offset:16384
	ds_read_b128 v[80:83], v142 offset:4096
	ds_read_b128 v[84:87], v143 offset:4096
	ds_read_b128 v[56:59], v140 offset:24576
	ds_read_b128 v[60:63], v141 offset:24576
	ds_read_b128 v[88:91], v142 offset:6144
	ds_read_b128 v[92:95], v143 offset:6144
	s_mov_b32 m0, s18
	s_mov_b64 s[46:47], s[8:9]
	global_load_lds_dwordx4 v1, s[46:47]
	s_add_u32 m0, m0, 0x1000
	s_add_u32 s46, s46, 0x1000
	s_addc_u32 s47, s47, 0
	global_load_lds_dwordx4 v1, s[46:47]
	s_add_u32 m0, m0, 0x1000
	s_add_u32 s46, s46, 0x1000
	s_addc_u32 s47, s47, 0
	global_load_lds_dwordx4 v1, s[46:47]
	s_add_u32 m0, m0, 0x1000
	s_add_u32 s46, s46, 0x1000
	s_addc_u32 s47, s47, 0
	global_load_lds_dwordx4 v1, s[46:47]
	s_add_u32 m0, m0, 0x1000
	s_add_u32 s46, s46, 0x1000
	s_addc_u32 s47, s47, 0
	global_load_lds_dwordx4 v1, s[46:47]
	s_add_u32 m0, m0, 0x1000
	s_add_u32 s46, s46, 0x1000
	s_addc_u32 s47, s47, 0
	global_load_lds_dwordx4 v1, s[46:47]
	s_add_u32 m0, m0, 0x1000
	s_add_u32 s46, s46, 0x1000
	s_addc_u32 s47, s47, 0
	global_load_lds_dwordx4 v1, s[46:47]
	s_add_u32 m0, m0, 0x1000
	s_add_u32 s46, s46, 0x1000
	s_addc_u32 s47, s47, 0
	global_load_lds_dwordx4 v1, s[46:47]
	s_add_u32 m0, m0, 0x1000
	s_mov_b64 s[46:47], s[10:11]
	s_nop 0
	global_load_lds_dwordx4 v2, s[46:47]
	s_add_u32 m0, m0, 0x1000
	s_add_u32 s46, s46, 0x10000
	s_addc_u32 s47, s47, 0
	global_load_lds_dwordx4 v2, s[46:47]
	s_add_u32 s8, s8, 0x8000
	s_addc_u32 s9, s9, 0
	s_add_u32 s10, s10, 0x20000
	s_addc_u32 s11, s11, 0
	s_waitcnt lgkmcnt(8)
	v_mfma_f32_16x16x32_bf16 v[128:131], v[10:13], v[32:35], 0
	v_mfma_f32_16x16x32_bf16 v[96:99], v[32:35], v[10:13], 0
	v_mfma_f32_16x16x32_bf16 v[128:131], v[10:13], v[36:39], v[128:131]
	v_mfma_f32_16x16x32_bf16 v[96:99], v[36:39], v[10:13], v[96:99]
	v_mfma_f32_16x16x32_bf16 v[132:135], v[10:13], v[40:43], 0
	v_mfma_f32_16x16x32_bf16 v[100:103], v[40:43], v[10:13], 0
	v_mfma_f32_16x16x32_bf16 v[132:135], v[10:13], v[44:47], v[132:135]
	v_mfma_f32_16x16x32_bf16 v[100:103], v[44:47], v[10:13], v[100:103]
	s_waitcnt lgkmcnt(4)
	v_mfma_f32_16x16x32_bf16 v[136:139], v[10:13], v[48:51], 0
	v_mfma_f32_16x16x32_bf16 v[104:107], v[48:51], v[10:13], 0
	v_mfma_f32_16x16x32_bf16 v[136:139], v[10:13], v[52:55], v[136:139]
	v_mfma_f32_16x16x32_bf16 v[104:107], v[52:55], v[10:13], v[104:107]
	s_waitcnt lgkmcnt(0)
	v_mfma_f32_16x16x32_bf16 v[140:143], v[10:13], v[56:59], 0
	v_mfma_f32_16x16x32_bf16 v[108:111], v[56:59], v[10:13], 0
	v_mfma_f32_16x16x32_bf16 v[140:143], v[10:13], v[60:63], v[140:143]
	v_mfma_f32_16x16x32_bf16 v[108:111], v[60:63], v[10:13], v[108:111]
	v_rcp_f32_e32 v146, v128
	v_lshlrev_b32_e32 v148, 16, v32
	v_and_b32_e32 v149, 0xffff0000, v32
	v_pk_mul_f32 v[148:149], v[148:149], v[146:147] op_sel_hi:[1,0]
	v_cvt_pk_f16_f32 v32, v148, v149
	v_lshlrev_b32_e32 v150, 16, v33
	v_and_b32_e32 v151, 0xffff0000, v33
	v_pk_mul_f32 v[150:151], v[150:151], v[146:147] op_sel_hi:[1,0]
	v_cvt_pk_f16_f32 v33, v150, v151
	v_lshlrev_b32_e32 v148, 16, v34
	v_and_b32_e32 v149, 0xffff0000, v34
	v_pk_mul_f32 v[148:149], v[148:149], v[146:147] op_sel_hi:[1,0]
	v_cvt_pk_f16_f32 v34, v148, v149
	v_lshlrev_b32_e32 v150, 16, v35
	v_and_b32_e32 v151, 0xffff0000, v35
	v_pk_mul_f32 v[150:151], v[150:151], v[146:147] op_sel_hi:[1,0]
	v_cvt_pk_f16_f32 v35, v150, v151
	v_lshlrev_b32_e32 v148, 16, v36
	v_and_b32_e32 v149, 0xffff0000, v36
	v_pk_mul_f32 v[148:149], v[148:149], v[146:147] op_sel_hi:[1,0]
	v_cvt_pk_f16_f32 v36, v148, v149
	v_lshlrev_b32_e32 v150, 16, v37
	v_and_b32_e32 v151, 0xffff0000, v37
	v_pk_mul_f32 v[150:151], v[150:151], v[146:147] op_sel_hi:[1,0]
	v_cvt_pk_f16_f32 v37, v150, v151
	v_lshlrev_b32_e32 v148, 16, v38
	v_and_b32_e32 v149, 0xffff0000, v38
	v_pk_mul_f32 v[148:149], v[148:149], v[146:147] op_sel_hi:[1,0]
	v_cvt_pk_f16_f32 v38, v148, v149
	v_lshlrev_b32_e32 v150, 16, v39
	v_and_b32_e32 v151, 0xffff0000, v39
	v_pk_mul_f32 v[150:151], v[150:151], v[146:147] op_sel_hi:[1,0]
	v_cvt_pk_f16_f32 v39, v150, v151
	s_nop 1
	v_mfma_f32_16x16x32_f16 v[112:115], v[32:35], v[64:67], 0
	v_mfma_f32_16x16x32_f16 v[112:115], v[36:39], v[68:71], v[112:115]
	v_rcp_f32_e32 v146, v132
	v_lshlrev_b32_e32 v148, 16, v40
	v_and_b32_e32 v149, 0xffff0000, v40
	v_pk_mul_f32 v[148:149], v[148:149], v[146:147] op_sel_hi:[1,0]
	v_cvt_pk_f16_f32 v40, v148, v149
	v_lshlrev_b32_e32 v150, 16, v41
	v_and_b32_e32 v151, 0xffff0000, v41
	v_pk_mul_f32 v[150:151], v[150:151], v[146:147] op_sel_hi:[1,0]
	v_cvt_pk_f16_f32 v41, v150, v151
	v_lshlrev_b32_e32 v148, 16, v42
	v_and_b32_e32 v149, 0xffff0000, v42
	v_pk_mul_f32 v[148:149], v[148:149], v[146:147] op_sel_hi:[1,0]
	v_cvt_pk_f16_f32 v42, v148, v149
	v_lshlrev_b32_e32 v150, 16, v43
	v_and_b32_e32 v151, 0xffff0000, v43
	v_pk_mul_f32 v[150:151], v[150:151], v[146:147] op_sel_hi:[1,0]
	v_cvt_pk_f16_f32 v43, v150, v151
	v_lshlrev_b32_e32 v148, 16, v44
	v_and_b32_e32 v149, 0xffff0000, v44
	v_pk_mul_f32 v[148:149], v[148:149], v[146:147] op_sel_hi:[1,0]
	v_cvt_pk_f16_f32 v44, v148, v149
	v_lshlrev_b32_e32 v150, 16, v45
	v_and_b32_e32 v151, 0xffff0000, v45
	v_pk_mul_f32 v[150:151], v[150:151], v[146:147] op_sel_hi:[1,0]
	v_cvt_pk_f16_f32 v45, v150, v151
	v_lshlrev_b32_e32 v148, 16, v46
	v_and_b32_e32 v149, 0xffff0000, v46
	v_pk_mul_f32 v[148:149], v[148:149], v[146:147] op_sel_hi:[1,0]
	v_cvt_pk_f16_f32 v46, v148, v149
	v_lshlrev_b32_e32 v150, 16, v47
	v_and_b32_e32 v151, 0xffff0000, v47
	v_pk_mul_f32 v[150:151], v[150:151], v[146:147] op_sel_hi:[1,0]
	v_cvt_pk_f16_f32 v47, v150, v151
	s_nop 1
	v_mfma_f32_16x16x32_f16 v[116:119], v[40:43], v[72:75], 0
	v_mfma_f32_16x16x32_f16 v[116:119], v[44:47], v[76:79], v[116:119]
	v_rcp_f32_e32 v146, v136
	v_lshlrev_b32_e32 v148, 16, v48
	v_and_b32_e32 v149, 0xffff0000, v48
	v_pk_mul_f32 v[148:149], v[148:149], v[146:147] op_sel_hi:[1,0]
	v_cvt_pk_f16_f32 v48, v148, v149
	v_lshlrev_b32_e32 v150, 16, v49
	v_and_b32_e32 v151, 0xffff0000, v49
	v_pk_mul_f32 v[150:151], v[150:151], v[146:147] op_sel_hi:[1,0]
	v_cvt_pk_f16_f32 v49, v150, v151
	v_lshlrev_b32_e32 v148, 16, v50
	v_and_b32_e32 v149, 0xffff0000, v50
	v_pk_mul_f32 v[148:149], v[148:149], v[146:147] op_sel_hi:[1,0]
	v_cvt_pk_f16_f32 v50, v148, v149
	v_lshlrev_b32_e32 v150, 16, v51
	v_and_b32_e32 v151, 0xffff0000, v51
	v_pk_mul_f32 v[150:151], v[150:151], v[146:147] op_sel_hi:[1,0]
	v_cvt_pk_f16_f32 v51, v150, v151
	v_lshlrev_b32_e32 v148, 16, v52
	v_and_b32_e32 v149, 0xffff0000, v52
	v_pk_mul_f32 v[148:149], v[148:149], v[146:147] op_sel_hi:[1,0]
	v_cvt_pk_f16_f32 v52, v148, v149
	v_lshlrev_b32_e32 v150, 16, v53
	v_and_b32_e32 v151, 0xffff0000, v53
	v_pk_mul_f32 v[150:151], v[150:151], v[146:147] op_sel_hi:[1,0]
	v_cvt_pk_f16_f32 v53, v150, v151
	v_lshlrev_b32_e32 v148, 16, v54
	v_and_b32_e32 v149, 0xffff0000, v54
	v_pk_mul_f32 v[148:149], v[148:149], v[146:147] op_sel_hi:[1,0]
	v_cvt_pk_f16_f32 v54, v148, v149
	v_lshlrev_b32_e32 v150, 16, v55
	v_and_b32_e32 v151, 0xffff0000, v55
	v_pk_mul_f32 v[150:151], v[150:151], v[146:147] op_sel_hi:[1,0]
	v_cvt_pk_f16_f32 v55, v150, v151
	s_nop 1
	v_mfma_f32_16x16x32_f16 v[120:123], v[48:51], v[80:83], 0
	v_mfma_f32_16x16x32_f16 v[120:123], v[52:55], v[84:87], v[120:123]
	v_rcp_f32_e32 v146, v140
	v_lshlrev_b32_e32 v148, 16, v56
	v_and_b32_e32 v149, 0xffff0000, v56
	v_pk_mul_f32 v[148:149], v[148:149], v[146:147] op_sel_hi:[1,0]
	v_cvt_pk_f16_f32 v56, v148, v149
	v_lshlrev_b32_e32 v150, 16, v57
	v_and_b32_e32 v151, 0xffff0000, v57
	v_pk_mul_f32 v[150:151], v[150:151], v[146:147] op_sel_hi:[1,0]
	v_cvt_pk_f16_f32 v57, v150, v151
	v_lshlrev_b32_e32 v148, 16, v58
	v_and_b32_e32 v149, 0xffff0000, v58
	v_pk_mul_f32 v[148:149], v[148:149], v[146:147] op_sel_hi:[1,0]
	v_cvt_pk_f16_f32 v58, v148, v149
	v_lshlrev_b32_e32 v150, 16, v59
	v_and_b32_e32 v151, 0xffff0000, v59
	v_pk_mul_f32 v[150:151], v[150:151], v[146:147] op_sel_hi:[1,0]
	v_cvt_pk_f16_f32 v59, v150, v151
	v_lshlrev_b32_e32 v148, 16, v60
	v_and_b32_e32 v149, 0xffff0000, v60
	v_pk_mul_f32 v[148:149], v[148:149], v[146:147] op_sel_hi:[1,0]
	v_cvt_pk_f16_f32 v60, v148, v149
	v_lshlrev_b32_e32 v150, 16, v61
	v_and_b32_e32 v151, 0xffff0000, v61
	v_pk_mul_f32 v[150:151], v[150:151], v[146:147] op_sel_hi:[1,0]
	v_cvt_pk_f16_f32 v61, v150, v151
	v_lshlrev_b32_e32 v148, 16, v62
	v_and_b32_e32 v149, 0xffff0000, v62
	v_pk_mul_f32 v[148:149], v[148:149], v[146:147] op_sel_hi:[1,0]
	v_cvt_pk_f16_f32 v62, v148, v149
	v_lshlrev_b32_e32 v150, 16, v63
	v_and_b32_e32 v151, 0xffff0000, v63
	v_pk_mul_f32 v[150:151], v[150:151], v[146:147] op_sel_hi:[1,0]
	v_cvt_pk_f16_f32 v63, v150, v151
	s_nop 1
	v_mfma_f32_16x16x32_f16 v[124:127], v[56:59], v[88:91], 0
	v_mfma_f32_16x16x32_f16 v[124:127], v[60:63], v[92:95], v[124:127]
	s_cmp_eq_u32 s6, 0
	s_cbranch_scc1 .Lsc_V_zver_l
	v_max_f32_e32 v144, 0x0da24260, v20
	v_max_f32_e32 v145, 0x0da24260, v21
	v_max_f32_e32 v156, 0x0da24260, v22
	v_max_f32_e32 v157, 0x0da24260, v23
	v_rcp_f32_e32 v144, v144
	v_rcp_f32_e32 v145, v145
	v_rcp_f32_e32 v156, v156
	v_rcp_f32_e32 v157, v157
	v_pk_mul_f32 v[144:145], v[16:17], v[144:145]
	v_pk_mul_f32 v[156:157], v[18:19], v[156:157]
	v_cvt_pk_f16_f32 v152, v144, v145
	v_cvt_pk_f16_f32 v153, v156, v157
	global_store_dwordx2 v7, v[152:153], s[12:13]
	v_pk_fma_f32 v[16:17], v[96:97], v[112:113], v[16:17]
	v_pk_fma_f32 v[18:19], v[98:99], v[114:115], v[18:19]
	v_pk_add_f32 v[20:21], v[20:21], v[96:97]
	v_pk_add_f32 v[22:23], v[22:23], v[98:99]
	v_max_f32_e32 v144, 0x0da24260, v20
	v_max_f32_e32 v145, 0x0da24260, v21
	v_max_f32_e32 v156, 0x0da24260, v22
	v_max_f32_e32 v157, 0x0da24260, v23
	v_rcp_f32_e32 v144, v144
	v_rcp_f32_e32 v145, v145
	v_rcp_f32_e32 v156, v156
	v_rcp_f32_e32 v157, v157
	v_pk_mul_f32 v[144:145], v[16:17], v[144:145]
	v_pk_mul_f32 v[156:157], v[18:19], v[156:157]
	v_cvt_pk_f16_f32 v154, v144, v145
	v_cvt_pk_f16_f32 v155, v156, v157
	global_store_dwordx2 v160, v[154:155], s[12:13]
	v_pk_fma_f32 v[16:17], v[100:101], v[116:117], v[16:17]
	v_pk_fma_f32 v[18:19], v[102:103], v[118:119], v[18:19]
	v_pk_add_f32 v[20:21], v[20:21], v[100:101]
	v_pk_add_f32 v[22:23], v[22:23], v[102:103]
	v_max_f32_e32 v144, 0x0da24260, v20
	v_max_f32_e32 v145, 0x0da24260, v21
	v_max_f32_e32 v156, 0x0da24260, v22
	v_max_f32_e32 v157, 0x0da24260, v23
	v_rcp_f32_e32 v144, v144
	v_rcp_f32_e32 v145, v145
	v_rcp_f32_e32 v156, v156
	v_rcp_f32_e32 v157, v157
	v_pk_mul_f32 v[144:145], v[16:17], v[144:145]
	v_pk_mul_f32 v[156:157], v[18:19], v[156:157]
	v_cvt_pk_f16_f32 v152, v144, v145
	v_cvt_pk_f16_f32 v153, v156, v157
	global_store_dwordx2 v161, v[152:153], s[12:13]
	v_pk_fma_f32 v[16:17], v[104:105], v[120:121], v[16:17]
	v_pk_fma_f32 v[18:19], v[106:107], v[122:123], v[18:19]
	v_pk_add_f32 v[20:21], v[20:21], v[104:105]
	v_pk_add_f32 v[22:23], v[22:23], v[106:107]
	v_max_f32_e32 v144, 0x0da24260, v20
	v_max_f32_e32 v145, 0x0da24260, v21
	v_max_f32_e32 v156, 0x0da24260, v22
	v_max_f32_e32 v157, 0x0da24260, v23
	v_rcp_f32_e32 v144, v144
	v_rcp_f32_e32 v145, v145
	v_rcp_f32_e32 v156, v156
	v_rcp_f32_e32 v157, v157
	v_pk_mul_f32 v[144:145], v[16:17], v[144:145]
	v_pk_mul_f32 v[156:157], v[18:19], v[156:157]
	v_cvt_pk_f16_f32 v154, v144, v145
	v_cvt_pk_f16_f32 v155, v156, v157
	global_store_dwordx2 v162, v[154:155], s[12:13]
	v_pk_fma_f32 v[16:17], v[108:109], v[124:125], v[16:17]
	v_pk_fma_f32 v[18:19], v[110:111], v[126:127], v[18:19]
	v_pk_add_f32 v[20:21], v[20:21], v[108:109]
	v_pk_add_f32 v[22:23], v[22:23], v[110:111]
	s_add_u32 s12, s12, 0x20000
	s_addc_u32 s13, s13, 0
	s_add_u32 s14, s14, 0x800
	s_addc_u32 s15, s15, 0
	s_branch .Lsc_V_seqdone_l
.Lsc_V_zver_l:
	v_max_f32_e32 v144, 0x0da24260, v20
	v_max_f32_e32 v145, 0x0da24260, v21
	v_max_f32_e32 v156, 0x0da24260, v22
	v_max_f32_e32 v157, 0x0da24260, v23
	v_rcp_f32_e32 v144, v144
	v_rcp_f32_e32 v145, v145
	v_rcp_f32_e32 v156, v156
	v_rcp_f32_e32 v157, v157
	v_pk_mul_f32 v[144:145], v[16:17], v[144:145]
	v_pk_mul_f32 v[156:157], v[18:19], v[156:157]
	v_cvt_pk_f16_f32 v152, v144, v145
	v_cvt_pk_f16_f32 v153, v156, v157
	global_store_dwordx2 v7, v[152:153], s[12:13]
	s_mov_b64 exec, s[20:21]
	global_store_dwordx4 v8, v[20:23], s[14:15]
	s_mov_b64 exec, -1
	v_pk_fma_f32 v[16:17], v[96:97], v[112:113], v[16:17]
	v_pk_fma_f32 v[18:19], v[98:99], v[114:115], v[18:19]
	v_pk_add_f32 v[20:21], v[20:21], v[96:97]
	v_pk_add_f32 v[22:23], v[22:23], v[98:99]
	v_max_f32_e32 v144, 0x0da24260, v20
	v_max_f32_e32 v145, 0x0da24260, v21
	v_max_f32_e32 v156, 0x0da24260, v22
	v_max_f32_e32 v157, 0x0da24260, v23
	v_rcp_f32_e32 v144, v144
	v_rcp_f32_e32 v145, v145
	v_rcp_f32_e32 v156, v156
	v_rcp_f32_e32 v157, v157
	v_pk_mul_f32 v[144:145], v[16:17], v[144:145]
	v_pk_mul_f32 v[156:157], v[18:19], v[156:157]
	v_cvt_pk_f16_f32 v154, v144, v145
	v_cvt_pk_f16_f32 v155, v156, v157
	global_store_dwordx2 v160, v[154:155], s[12:13]
	s_mov_b64 exec, s[20:21]
	global_store_dwordx4 v8, v[20:23], s[14:15] offset:512
	s_mov_b64 exec, -1
	v_pk_fma_f32 v[16:17], v[100:101], v[116:117], v[16:17]
	v_pk_fma_f32 v[18:19], v[102:103], v[118:119], v[18:19]
	v_pk_add_f32 v[20:21], v[20:21], v[100:101]
	v_pk_add_f32 v[22:23], v[22:23], v[102:103]
	v_max_f32_e32 v144, 0x0da24260, v20
	v_max_f32_e32 v145, 0x0da24260, v21
	v_max_f32_e32 v156, 0x0da24260, v22
	v_max_f32_e32 v157, 0x0da24260, v23
	v_rcp_f32_e32 v144, v144
	v_rcp_f32_e32 v145, v145
	v_rcp_f32_e32 v156, v156
	v_rcp_f32_e32 v157, v157
	v_pk_mul_f32 v[144:145], v[16:17], v[144:145]
	v_pk_mul_f32 v[156:157], v[18:19], v[156:157]
	v_cvt_pk_f16_f32 v152, v144, v145
	v_cvt_pk_f16_f32 v153, v156, v157
	global_store_dwordx2 v161, v[152:153], s[12:13]
	s_mov_b64 exec, s[20:21]
	global_store_dwordx4 v8, v[20:23], s[14:15] offset:1024
	s_mov_b64 exec, -1
	v_pk_fma_f32 v[16:17], v[104:105], v[120:121], v[16:17]
	v_pk_fma_f32 v[18:19], v[106:107], v[122:123], v[18:19]
	v_pk_add_f32 v[20:21], v[20:21], v[104:105]
	v_pk_add_f32 v[22:23], v[22:23], v[106:107]
	v_max_f32_e32 v144, 0x0da24260, v20
	v_max_f32_e32 v145, 0x0da24260, v21
	v_max_f32_e32 v156, 0x0da24260, v22
	v_max_f32_e32 v157, 0x0da24260, v23
	v_rcp_f32_e32 v144, v144
	v_rcp_f32_e32 v145, v145
	v_rcp_f32_e32 v156, v156
	v_rcp_f32_e32 v157, v157
	v_pk_mul_f32 v[144:145], v[16:17], v[144:145]
	v_pk_mul_f32 v[156:157], v[18:19], v[156:157]
	v_cvt_pk_f16_f32 v154, v144, v145
	v_cvt_pk_f16_f32 v155, v156, v157
	global_store_dwordx2 v162, v[154:155], s[12:13]
	s_mov_b64 exec, s[20:21]
	global_store_dwordx4 v8, v[20:23], s[14:15] offset:1536
	s_mov_b64 exec, -1
	v_pk_fma_f32 v[16:17], v[108:109], v[124:125], v[16:17]
	v_pk_fma_f32 v[18:19], v[110:111], v[126:127], v[18:19]
	v_pk_add_f32 v[20:21], v[20:21], v[108:109]
	v_pk_add_f32 v[22:23], v[22:23], v[110:111]
	s_add_u32 s12, s12, 0x20000
	s_addc_u32 s13, s13, 0
	s_add_u32 s14, s14, 0x800
	s_addc_u32 s15, s15, 0
.Lsc_V_seqdone_l:
	s_add_u32 s16, s16, 1
	s_and_b32 s44, s16, 3
	s_mul_i32 s17, s44, 40960
	s_add_u32 s44, s16, 3
	s_and_b32 s44, s44, 3
	s_mul_i32 s44, s44, 40960
	s_add_u32 s18, s44, s19
	s_cmp_lt_u32 s16, 5
	s_cbranch_scc1 .Lsc_V_loop
	s_mov_b32 s17, 40960
	s_waitcnt vmcnt(32)
	s_barrier
	v_add_u32_e32 v140, s17, v3
	v_add_u32_e32 v141, s17, v4
	v_add_u32_e32 v142, s17, v5
	v_add_u32_e32 v143, s17, v6
	ds_read_b128 v[32:35], v140 offset:0
	ds_read_b128 v[36:39], v141 offset:0
	ds_read_b128 v[64:67], v142 offset:0
	ds_read_b128 v[68:71], v143 offset:0
	ds_read_b128 v[40:43], v140 offset:8192
	ds_read_b128 v[44:47], v141 offset:8192
	ds_read_b128 v[72:75], v142 offset:2048
	ds_read_b128 v[76:79], v143 offset:2048
	ds_read_b128 v[48:51], v140 offset:16384
	ds_read_b128 v[52:55], v141 offset:16384
	ds_read_b128 v[80:83], v142 offset:4096
	ds_read_b128 v[84:87], v143 offset:4096
	ds_read_b128 v[56:59], v140 offset:24576
	ds_read_b128 v[60:63], v141 offset:24576
	ds_read_b128 v[88:91], v142 offset:6144
	ds_read_b128 v[92:95], v143 offset:6144
	s_waitcnt lgkmcnt(8)
	v_mfma_f32_16x16x32_bf16 v[128:131], v[10:13], v[32:35], 0
	v_mfma_f32_16x16x32_bf16 v[96:99], v[32:35], v[10:13], 0
	v_mfma_f32_16x16x32_bf16 v[128:131], v[10:13], v[36:39], v[128:131]
	v_mfma_f32_16x16x32_bf16 v[96:99], v[36:39], v[10:13], v[96:99]
	v_mfma_f32_16x16x32_bf16 v[132:135], v[10:13], v[40:43], 0
	v_mfma_f32_16x16x32_bf16 v[100:103], v[40:43], v[10:13], 0
	v_mfma_f32_16x16x32_bf16 v[132:135], v[10:13], v[44:47], v[132:135]
	v_mfma_f32_16x16x32_bf16 v[100:103], v[44:47], v[10:13], v[100:103]
	s_waitcnt lgkmcnt(4)
	v_mfma_f32_16x16x32_bf16 v[136:139], v[10:13], v[48:51], 0
	v_mfma_f32_16x16x32_bf16 v[104:107], v[48:51], v[10:13], 0
	v_mfma_f32_16x16x32_bf16 v[136:139], v[10:13], v[52:55], v[136:139]
	v_mfma_f32_16x16x32_bf16 v[104:107], v[52:55], v[10:13], v[104:107]
	s_waitcnt lgkmcnt(0)
	v_mfma_f32_16x16x32_bf16 v[140:143], v[10:13], v[56:59], 0
	v_mfma_f32_16x16x32_bf16 v[108:111], v[56:59], v[10:13], 0
	v_mfma_f32_16x16x32_bf16 v[140:143], v[10:13], v[60:63], v[140:143]
	v_mfma_f32_16x16x32_bf16 v[108:111], v[60:63], v[10:13], v[108:111]
	v_rcp_f32_e32 v146, v128
	v_lshlrev_b32_e32 v148, 16, v32
	v_and_b32_e32 v149, 0xffff0000, v32
	v_pk_mul_f32 v[148:149], v[148:149], v[146:147] op_sel_hi:[1,0]
	v_cvt_pk_f16_f32 v32, v148, v149
	v_lshlrev_b32_e32 v150, 16, v33
	v_and_b32_e32 v151, 0xffff0000, v33
	v_pk_mul_f32 v[150:151], v[150:151], v[146:147] op_sel_hi:[1,0]
	v_cvt_pk_f16_f32 v33, v150, v151
	v_lshlrev_b32_e32 v148, 16, v34
	v_and_b32_e32 v149, 0xffff0000, v34
	v_pk_mul_f32 v[148:149], v[148:149], v[146:147] op_sel_hi:[1,0]
	v_cvt_pk_f16_f32 v34, v148, v149
	v_lshlrev_b32_e32 v150, 16, v35
	v_and_b32_e32 v151, 0xffff0000, v35
	v_pk_mul_f32 v[150:151], v[150:151], v[146:147] op_sel_hi:[1,0]
	v_cvt_pk_f16_f32 v35, v150, v151
	v_lshlrev_b32_e32 v148, 16, v36
	v_and_b32_e32 v149, 0xffff0000, v36
	v_pk_mul_f32 v[148:149], v[148:149], v[146:147] op_sel_hi:[1,0]
	v_cvt_pk_f16_f32 v36, v148, v149
	v_lshlrev_b32_e32 v150, 16, v37
	v_and_b32_e32 v151, 0xffff0000, v37
	v_pk_mul_f32 v[150:151], v[150:151], v[146:147] op_sel_hi:[1,0]
	v_cvt_pk_f16_f32 v37, v150, v151
	v_lshlrev_b32_e32 v148, 16, v38
	v_and_b32_e32 v149, 0xffff0000, v38
	v_pk_mul_f32 v[148:149], v[148:149], v[146:147] op_sel_hi:[1,0]
	v_cvt_pk_f16_f32 v38, v148, v149
	v_lshlrev_b32_e32 v150, 16, v39
	v_and_b32_e32 v151, 0xffff0000, v39
	v_pk_mul_f32 v[150:151], v[150:151], v[146:147] op_sel_hi:[1,0]
	v_cvt_pk_f16_f32 v39, v150, v151
	s_nop 1
	v_mfma_f32_16x16x32_f16 v[112:115], v[32:35], v[64:67], 0
	v_mfma_f32_16x16x32_f16 v[112:115], v[36:39], v[68:71], v[112:115]
	v_rcp_f32_e32 v146, v132
	v_lshlrev_b32_e32 v148, 16, v40
	v_and_b32_e32 v149, 0xffff0000, v40
	v_pk_mul_f32 v[148:149], v[148:149], v[146:147] op_sel_hi:[1,0]
	v_cvt_pk_f16_f32 v40, v148, v149
	v_lshlrev_b32_e32 v150, 16, v41
	v_and_b32_e32 v151, 0xffff0000, v41
	v_pk_mul_f32 v[150:151], v[150:151], v[146:147] op_sel_hi:[1,0]
	v_cvt_pk_f16_f32 v41, v150, v151
	v_lshlrev_b32_e32 v148, 16, v42
	v_and_b32_e32 v149, 0xffff0000, v42
	v_pk_mul_f32 v[148:149], v[148:149], v[146:147] op_sel_hi:[1,0]
	v_cvt_pk_f16_f32 v42, v148, v149
	v_lshlrev_b32_e32 v150, 16, v43
	v_and_b32_e32 v151, 0xffff0000, v43
	v_pk_mul_f32 v[150:151], v[150:151], v[146:147] op_sel_hi:[1,0]
	v_cvt_pk_f16_f32 v43, v150, v151
	v_lshlrev_b32_e32 v148, 16, v44
	v_and_b32_e32 v149, 0xffff0000, v44
	v_pk_mul_f32 v[148:149], v[148:149], v[146:147] op_sel_hi:[1,0]
	v_cvt_pk_f16_f32 v44, v148, v149
	v_lshlrev_b32_e32 v150, 16, v45
	v_and_b32_e32 v151, 0xffff0000, v45
	v_pk_mul_f32 v[150:151], v[150:151], v[146:147] op_sel_hi:[1,0]
	v_cvt_pk_f16_f32 v45, v150, v151
	v_lshlrev_b32_e32 v148, 16, v46
	v_and_b32_e32 v149, 0xffff0000, v46
	v_pk_mul_f32 v[148:149], v[148:149], v[146:147] op_sel_hi:[1,0]
	v_cvt_pk_f16_f32 v46, v148, v149
	v_lshlrev_b32_e32 v150, 16, v47
	v_and_b32_e32 v151, 0xffff0000, v47
	v_pk_mul_f32 v[150:151], v[150:151], v[146:147] op_sel_hi:[1,0]
	v_cvt_pk_f16_f32 v47, v150, v151
	s_nop 1
	v_mfma_f32_16x16x32_f16 v[116:119], v[40:43], v[72:75], 0
	v_mfma_f32_16x16x32_f16 v[116:119], v[44:47], v[76:79], v[116:119]
	v_rcp_f32_e32 v146, v136
	v_lshlrev_b32_e32 v148, 16, v48
	v_and_b32_e32 v149, 0xffff0000, v48
	v_pk_mul_f32 v[148:149], v[148:149], v[146:147] op_sel_hi:[1,0]
	v_cvt_pk_f16_f32 v48, v148, v149
	v_lshlrev_b32_e32 v150, 16, v49
	v_and_b32_e32 v151, 0xffff0000, v49
	v_pk_mul_f32 v[150:151], v[150:151], v[146:147] op_sel_hi:[1,0]
	v_cvt_pk_f16_f32 v49, v150, v151
	v_lshlrev_b32_e32 v148, 16, v50
	v_and_b32_e32 v149, 0xffff0000, v50
	v_pk_mul_f32 v[148:149], v[148:149], v[146:147] op_sel_hi:[1,0]
	v_cvt_pk_f16_f32 v50, v148, v149
	v_lshlrev_b32_e32 v150, 16, v51
	v_and_b32_e32 v151, 0xffff0000, v51
	v_pk_mul_f32 v[150:151], v[150:151], v[146:147] op_sel_hi:[1,0]
	v_cvt_pk_f16_f32 v51, v150, v151
	v_lshlrev_b32_e32 v148, 16, v52
	v_and_b32_e32 v149, 0xffff0000, v52
	v_pk_mul_f32 v[148:149], v[148:149], v[146:147] op_sel_hi:[1,0]
	v_cvt_pk_f16_f32 v52, v148, v149
	v_lshlrev_b32_e32 v150, 16, v53
	v_and_b32_e32 v151, 0xffff0000, v53
	v_pk_mul_f32 v[150:151], v[150:151], v[146:147] op_sel_hi:[1,0]
	v_cvt_pk_f16_f32 v53, v150, v151
	v_lshlrev_b32_e32 v148, 16, v54
	v_and_b32_e32 v149, 0xffff0000, v54
	v_pk_mul_f32 v[148:149], v[148:149], v[146:147] op_sel_hi:[1,0]
	v_cvt_pk_f16_f32 v54, v148, v149
	v_lshlrev_b32_e32 v150, 16, v55
	v_and_b32_e32 v151, 0xffff0000, v55
	v_pk_mul_f32 v[150:151], v[150:151], v[146:147] op_sel_hi:[1,0]
	v_cvt_pk_f16_f32 v55, v150, v151
	s_nop 1
	v_mfma_f32_16x16x32_f16 v[120:123], v[48:51], v[80:83], 0
	v_mfma_f32_16x16x32_f16 v[120:123], v[52:55], v[84:87], v[120:123]
	v_rcp_f32_e32 v146, v140
	v_lshlrev_b32_e32 v148, 16, v56
	v_and_b32_e32 v149, 0xffff0000, v56
	v_pk_mul_f32 v[148:149], v[148:149], v[146:147] op_sel_hi:[1,0]
	v_cvt_pk_f16_f32 v56, v148, v149
	v_lshlrev_b32_e32 v150, 16, v57
	v_and_b32_e32 v151, 0xffff0000, v57
	v_pk_mul_f32 v[150:151], v[150:151], v[146:147] op_sel_hi:[1,0]
	v_cvt_pk_f16_f32 v57, v150, v151
	v_lshlrev_b32_e32 v148, 16, v58
	v_and_b32_e32 v149, 0xffff0000, v58
	v_pk_mul_f32 v[148:149], v[148:149], v[146:147] op_sel_hi:[1,0]
	v_cvt_pk_f16_f32 v58, v148, v149
	v_lshlrev_b32_e32 v150, 16, v59
	v_and_b32_e32 v151, 0xffff0000, v59
	v_pk_mul_f32 v[150:151], v[150:151], v[146:147] op_sel_hi:[1,0]
	v_cvt_pk_f16_f32 v59, v150, v151
	v_lshlrev_b32_e32 v148, 16, v60
	v_and_b32_e32 v149, 0xffff0000, v60
	v_pk_mul_f32 v[148:149], v[148:149], v[146:147] op_sel_hi:[1,0]
	v_cvt_pk_f16_f32 v60, v148, v149
	v_lshlrev_b32_e32 v150, 16, v61
	v_and_b32_e32 v151, 0xffff0000, v61
	v_pk_mul_f32 v[150:151], v[150:151], v[146:147] op_sel_hi:[1,0]
	v_cvt_pk_f16_f32 v61, v150, v151
	v_lshlrev_b32_e32 v148, 16, v62
	v_and_b32_e32 v149, 0xffff0000, v62
	v_pk_mul_f32 v[148:149], v[148:149], v[146:147] op_sel_hi:[1,0]
	v_cvt_pk_f16_f32 v62, v148, v149
	v_lshlrev_b32_e32 v150, 16, v63
	v_and_b32_e32 v151, 0xffff0000, v63
	v_pk_mul_f32 v[150:151], v[150:151], v[146:147] op_sel_hi:[1,0]
	v_cvt_pk_f16_f32 v63, v150, v151
	s_nop 1
	v_mfma_f32_16x16x32_f16 v[124:127], v[56:59], v[88:91], 0
	v_mfma_f32_16x16x32_f16 v[124:127], v[60:63], v[92:95], v[124:127]
	s_cmp_eq_u32 s6, 0
	s_cbranch_scc1 .Lsc_V_zver_t5
	v_max_f32_e32 v144, 0x0da24260, v20
	v_max_f32_e32 v145, 0x0da24260, v21
	v_max_f32_e32 v156, 0x0da24260, v22
	v_max_f32_e32 v157, 0x0da24260, v23
	v_rcp_f32_e32 v144, v144
	v_rcp_f32_e32 v145, v145
	v_rcp_f32_e32 v156, v156
	v_rcp_f32_e32 v157, v157
	v_pk_mul_f32 v[144:145], v[16:17], v[144:145]
	v_pk_mul_f32 v[156:157], v[18:19], v[156:157]
	v_cvt_pk_f16_f32 v152, v144, v145
	v_cvt_pk_f16_f32 v153, v156, v157
	global_store_dwordx2 v7, v[152:153], s[12:13]
	v_pk_fma_f32 v[16:17], v[96:97], v[112:113], v[16:17]
	v_pk_fma_f32 v[18:19], v[98:99], v[114:115], v[18:19]
	v_pk_add_f32 v[20:21], v[20:21], v[96:97]
	v_pk_add_f32 v[22:23], v[22:23], v[98:99]
	v_max_f32_e32 v144, 0x0da24260, v20
	v_max_f32_e32 v145, 0x0da24260, v21
	v_max_f32_e32 v156, 0x0da24260, v22
	v_max_f32_e32 v157, 0x0da24260, v23
	v_rcp_f32_e32 v144, v144
	v_rcp_f32_e32 v145, v145
	v_rcp_f32_e32 v156, v156
	v_rcp_f32_e32 v157, v157
	v_pk_mul_f32 v[144:145], v[16:17], v[144:145]
	v_pk_mul_f32 v[156:157], v[18:19], v[156:157]
	v_cvt_pk_f16_f32 v154, v144, v145
	v_cvt_pk_f16_f32 v155, v156, v157
	global_store_dwordx2 v160, v[154:155], s[12:13]
	v_pk_fma_f32 v[16:17], v[100:101], v[116:117], v[16:17]
	v_pk_fma_f32 v[18:19], v[102:103], v[118:119], v[18:19]
	v_pk_add_f32 v[20:21], v[20:21], v[100:101]
	v_pk_add_f32 v[22:23], v[22:23], v[102:103]
	v_max_f32_e32 v144, 0x0da24260, v20
	v_max_f32_e32 v145, 0x0da24260, v21
	v_max_f32_e32 v156, 0x0da24260, v22
	v_max_f32_e32 v157, 0x0da24260, v23
	v_rcp_f32_e32 v144, v144
	v_rcp_f32_e32 v145, v145
	v_rcp_f32_e32 v156, v156
	v_rcp_f32_e32 v157, v157
	v_pk_mul_f32 v[144:145], v[16:17], v[144:145]
	v_pk_mul_f32 v[156:157], v[18:19], v[156:157]
	v_cvt_pk_f16_f32 v152, v144, v145
	v_cvt_pk_f16_f32 v153, v156, v157
	global_store_dwordx2 v161, v[152:153], s[12:13]
	v_pk_fma_f32 v[16:17], v[104:105], v[120:121], v[16:17]
	v_pk_fma_f32 v[18:19], v[106:107], v[122:123], v[18:19]
	v_pk_add_f32 v[20:21], v[20:21], v[104:105]
	v_pk_add_f32 v[22:23], v[22:23], v[106:107]
	v_max_f32_e32 v144, 0x0da24260, v20
	v_max_f32_e32 v145, 0x0da24260, v21
	v_max_f32_e32 v156, 0x0da24260, v22
	v_max_f32_e32 v157, 0x0da24260, v23
	v_rcp_f32_e32 v144, v144
	v_rcp_f32_e32 v145, v145
	v_rcp_f32_e32 v156, v156
	v_rcp_f32_e32 v157, v157
	v_pk_mul_f32 v[144:145], v[16:17], v[144:145]
	v_pk_mul_f32 v[156:157], v[18:19], v[156:157]
	v_cvt_pk_f16_f32 v154, v144, v145
	v_cvt_pk_f16_f32 v155, v156, v157
	global_store_dwordx2 v162, v[154:155], s[12:13]
	v_pk_fma_f32 v[16:17], v[108:109], v[124:125], v[16:17]
	v_pk_fma_f32 v[18:19], v[110:111], v[126:127], v[18:19]
	v_pk_add_f32 v[20:21], v[20:21], v[108:109]
	v_pk_add_f32 v[22:23], v[22:23], v[110:111]
	s_add_u32 s12, s12, 0x20000
	s_addc_u32 s13, s13, 0
	s_add_u32 s14, s14, 0x800
	s_addc_u32 s15, s15, 0
	s_branch .Lsc_V_seqdone_t5

.Lsc_V_seqdone_t5:
	s_mov_b32 s17, 81920
	s_waitcnt vmcnt(22)
	s_barrier
	v_add_u32_e32 v140, s17, v3
	v_add_u32_e32 v141, s17, v4
	v_add_u32_e32 v142, s17, v5
	v_add_u32_e32 v143, s17, v6
	ds_read_b128 v[32:35], v140 offset:0
	ds_read_b128 v[36:39], v141 offset:0
	ds_read_b128 v[64:67], v142 offset:0
	ds_read_b128 v[68:71], v143 offset:0
	ds_read_b128 v[40:43], v140 offset:8192
	ds_read_b128 v[44:47], v141 offset:8192
	ds_read_b128 v[72:75], v142 offset:2048
	ds_read_b128 v[76:79], v143 offset:2048
	ds_read_b128 v[48:51], v140 offset:16384
	ds_read_b128 v[52:55], v141 offset:16384
	ds_read_b128 v[80:83], v142 offset:4096
	ds_read_b128 v[84:87], v143 offset:4096
	ds_read_b128 v[56:59], v140 offset:24576
	ds_read_b128 v[60:63], v141 offset:24576
	ds_read_b128 v[88:91], v142 offset:6144
	ds_read_b128 v[92:95], v143 offset:6144
	s_waitcnt lgkmcnt(8)
	v_mfma_f32_16x16x32_bf16 v[128:131], v[10:13], v[32:35], 0
	v_mfma_f32_16x16x32_bf16 v[96:99], v[32:35], v[10:13], 0
	v_mfma_f32_16x16x32_bf16 v[128:131], v[10:13], v[36:39], v[128:131]
	v_mfma_f32_16x16x32_bf16 v[96:99], v[36:39], v[10:13], v[96:99]
	v_mfma_f32_16x16x32_bf16 v[132:135], v[10:13], v[40:43], 0
	v_mfma_f32_16x16x32_bf16 v[100:103], v[40:43], v[10:13], 0
	v_mfma_f32_16x16x32_bf16 v[132:135], v[10:13], v[44:47], v[132:135]
	v_mfma_f32_16x16x32_bf16 v[100:103], v[44:47], v[10:13], v[100:103]
	s_waitcnt lgkmcnt(4)
	v_mfma_f32_16x16x32_bf16 v[136:139], v[10:13], v[48:51], 0
	v_mfma_f32_16x16x32_bf16 v[104:107], v[48:51], v[10:13], 0
	v_mfma_f32_16x16x32_bf16 v[136:139], v[10:13], v[52:55], v[136:139]
	v_mfma_f32_16x16x32_bf16 v[104:107], v[52:55], v[10:13], v[104:107]
	s_waitcnt lgkmcnt(0)
	v_mfma_f32_16x16x32_bf16 v[140:143], v[10:13], v[56:59], 0
	v_mfma_f32_16x16x32_bf16 v[108:111], v[56:59], v[10:13], 0
	v_mfma_f32_16x16x32_bf16 v[140:143], v[10:13], v[60:63], v[140:143]
	v_mfma_f32_16x16x32_bf16 v[108:111], v[60:63], v[10:13], v[108:111]
	v_rcp_f32_e32 v146, v128
	v_lshlrev_b32_e32 v148, 16, v32
	v_and_b32_e32 v149, 0xffff0000, v32
	v_pk_mul_f32 v[148:149], v[148:149], v[146:147] op_sel_hi:[1,0]
	v_cvt_pk_f16_f32 v32, v148, v149
	v_lshlrev_b32_e32 v150, 16, v33
	v_and_b32_e32 v151, 0xffff0000, v33
	v_pk_mul_f32 v[150:151], v[150:151], v[146:147] op_sel_hi:[1,0]
	v_cvt_pk_f16_f32 v33, v150, v151
	v_lshlrev_b32_e32 v148, 16, v34
	v_and_b32_e32 v149, 0xffff0000, v34
	v_pk_mul_f32 v[148:149], v[148:149], v[146:147] op_sel_hi:[1,0]
	v_cvt_pk_f16_f32 v34, v148, v149
	v_lshlrev_b32_e32 v150, 16, v35
	v_and_b32_e32 v151, 0xffff0000, v35
	v_pk_mul_f32 v[150:151], v[150:151], v[146:147] op_sel_hi:[1,0]
	v_cvt_pk_f16_f32 v35, v150, v151
	v_lshlrev_b32_e32 v148, 16, v36
	v_and_b32_e32 v149, 0xffff0000, v36
	v_pk_mul_f32 v[148:149], v[148:149], v[146:147] op_sel_hi:[1,0]
	v_cvt_pk_f16_f32 v36, v148, v149
	v_lshlrev_b32_e32 v150, 16, v37
	v_and_b32_e32 v151, 0xffff0000, v37
	v_pk_mul_f32 v[150:151], v[150:151], v[146:147] op_sel_hi:[1,0]
	v_cvt_pk_f16_f32 v37, v150, v151
	v_lshlrev_b32_e32 v148, 16, v38
	v_and_b32_e32 v149, 0xffff0000, v38
	v_pk_mul_f32 v[148:149], v[148:149], v[146:147] op_sel_hi:[1,0]
	v_cvt_pk_f16_f32 v38, v148, v149
	v_lshlrev_b32_e32 v150, 16, v39
	v_and_b32_e32 v151, 0xffff0000, v39
	v_pk_mul_f32 v[150:151], v[150:151], v[146:147] op_sel_hi:[1,0]
	v_cvt_pk_f16_f32 v39, v150, v151
	s_nop 1
	v_mfma_f32_16x16x32_f16 v[112:115], v[32:35], v[64:67], 0
	v_mfma_f32_16x16x32_f16 v[112:115], v[36:39], v[68:71], v[112:115]
	v_rcp_f32_e32 v146, v132
	v_lshlrev_b32_e32 v148, 16, v40
	v_and_b32_e32 v149, 0xffff0000, v40
	v_pk_mul_f32 v[148:149], v[148:149], v[146:147] op_sel_hi:[1,0]
	v_cvt_pk_f16_f32 v40, v148, v149
	v_lshlrev_b32_e32 v150, 16, v41
	v_and_b32_e32 v151, 0xffff0000, v41
	v_pk_mul_f32 v[150:151], v[150:151], v[146:147] op_sel_hi:[1,0]
	v_cvt_pk_f16_f32 v41, v150, v151
	v_lshlrev_b32_e32 v148, 16, v42
	v_and_b32_e32 v149, 0xffff0000, v42
	v_pk_mul_f32 v[148:149], v[148:149], v[146:147] op_sel_hi:[1,0]
	v_cvt_pk_f16_f32 v42, v148, v149
	v_lshlrev_b32_e32 v150, 16, v43
	v_and_b32_e32 v151, 0xffff0000, v43
	v_pk_mul_f32 v[150:151], v[150:151], v[146:147] op_sel_hi:[1,0]
	v_cvt_pk_f16_f32 v43, v150, v151
	v_lshlrev_b32_e32 v148, 16, v44
	v_and_b32_e32 v149, 0xffff0000, v44
	v_pk_mul_f32 v[148:149], v[148:149], v[146:147] op_sel_hi:[1,0]
	v_cvt_pk_f16_f32 v44, v148, v149
	v_lshlrev_b32_e32 v150, 16, v45
	v_and_b32_e32 v151, 0xffff0000, v45
	v_pk_mul_f32 v[150:151], v[150:151], v[146:147] op_sel_hi:[1,0]
	v_cvt_pk_f16_f32 v45, v150, v151
	v_lshlrev_b32_e32 v148, 16, v46
	v_and_b32_e32 v149, 0xffff0000, v46
	v_pk_mul_f32 v[148:149], v[148:149], v[146:147] op_sel_hi:[1,0]
	v_cvt_pk_f16_f32 v46, v148, v149
	v_lshlrev_b32_e32 v150, 16, v47
	v_and_b32_e32 v151, 0xffff0000, v47
	v_pk_mul_f32 v[150:151], v[150:151], v[146:147] op_sel_hi:[1,0]
	v_cvt_pk_f16_f32 v47, v150, v151
	s_nop 1
	v_mfma_f32_16x16x32_f16 v[116:119], v[40:43], v[72:75], 0
	v_mfma_f32_16x16x32_f16 v[116:119], v[44:47], v[76:79], v[116:119]
	v_rcp_f32_e32 v146, v136
	v_lshlrev_b32_e32 v148, 16, v48
	v_and_b32_e32 v149, 0xffff0000, v48
	v_pk_mul_f32 v[148:149], v[148:149], v[146:147] op_sel_hi:[1,0]
	v_cvt_pk_f16_f32 v48, v148, v149
	v_lshlrev_b32_e32 v150, 16, v49
	v_and_b32_e32 v151, 0xffff0000, v49
	v_pk_mul_f32 v[150:151], v[150:151], v[146:147] op_sel_hi:[1,0]
	v_cvt_pk_f16_f32 v49, v150, v151
	v_lshlrev_b32_e32 v148, 16, v50
	v_and_b32_e32 v149, 0xffff0000, v50
	v_pk_mul_f32 v[148:149], v[148:149], v[146:147] op_sel_hi:[1,0]
	v_cvt_pk_f16_f32 v50, v148, v149
	v_lshlrev_b32_e32 v150, 16, v51
	v_and_b32_e32 v151, 0xffff0000, v51
	v_pk_mul_f32 v[150:151], v[150:151], v[146:147] op_sel_hi:[1,0]
	v_cvt_pk_f16_f32 v51, v150, v151
	v_lshlrev_b32_e32 v148, 16, v52
	v_and_b32_e32 v149, 0xffff0000, v52
	v_pk_mul_f32 v[148:149], v[148:149], v[146:147] op_sel_hi:[1,0]
	v_cvt_pk_f16_f32 v52, v148, v149
	v_lshlrev_b32_e32 v150, 16, v53
	v_and_b32_e32 v151, 0xffff0000, v53
	v_pk_mul_f32 v[150:151], v[150:151], v[146:147] op_sel_hi:[1,0]
	v_cvt_pk_f16_f32 v53, v150, v151
	v_lshlrev_b32_e32 v148, 16, v54
	v_and_b32_e32 v149, 0xffff0000, v54
	v_pk_mul_f32 v[148:149], v[148:149], v[146:147] op_sel_hi:[1,0]
	v_cvt_pk_f16_f32 v54, v148, v149
	v_lshlrev_b32_e32 v150, 16, v55
	v_and_b32_e32 v151, 0xffff0000, v55
	v_pk_mul_f32 v[150:151], v[150:151], v[146:147] op_sel_hi:[1,0]
	v_cvt_pk_f16_f32 v55, v150, v151
	s_nop 1
	v_mfma_f32_16x16x32_f16 v[120:123], v[48:51], v[80:83], 0
	v_mfma_f32_16x16x32_f16 v[120:123], v[52:55], v[84:87], v[120:123]
	v_rcp_f32_e32 v146, v140
	v_lshlrev_b32_e32 v148, 16, v56
	v_and_b32_e32 v149, 0xffff0000, v56
	v_pk_mul_f32 v[148:149], v[148:149], v[146:147] op_sel_hi:[1,0]
	v_cvt_pk_f16_f32 v56, v148, v149
	v_lshlrev_b32_e32 v150, 16, v57
	v_and_b32_e32 v151, 0xffff0000, v57
	v_pk_mul_f32 v[150:151], v[150:151], v[146:147] op_sel_hi:[1,0]
	v_cvt_pk_f16_f32 v57, v150, v151
	v_lshlrev_b32_e32 v148, 16, v58
	v_and_b32_e32 v149, 0xffff0000, v58
	v_pk_mul_f32 v[148:149], v[148:149], v[146:147] op_sel_hi:[1,0]
	v_cvt_pk_f16_f32 v58, v148, v149
	v_lshlrev_b32_e32 v150, 16, v59
	v_and_b32_e32 v151, 0xffff0000, v59
	v_pk_mul_f32 v[150:151], v[150:151], v[146:147] op_sel_hi:[1,0]
	v_cvt_pk_f16_f32 v59, v150, v151
	v_lshlrev_b32_e32 v148, 16, v60
	v_and_b32_e32 v149, 0xffff0000, v60
	v_pk_mul_f32 v[148:149], v[148:149], v[146:147] op_sel_hi:[1,0]
	v_cvt_pk_f16_f32 v60, v148, v149
	v_lshlrev_b32_e32 v150, 16, v61
	v_and_b32_e32 v151, 0xffff0000, v61
	v_pk_mul_f32 v[150:151], v[150:151], v[146:147] op_sel_hi:[1,0]
	v_cvt_pk_f16_f32 v61, v150, v151
	v_lshlrev_b32_e32 v148, 16, v62
	v_and_b32_e32 v149, 0xffff0000, v62
	v_pk_mul_f32 v[148:149], v[148:149], v[146:147] op_sel_hi:[1,0]
	v_cvt_pk_f16_f32 v62, v148, v149
	v_lshlrev_b32_e32 v150, 16, v63
	v_and_b32_e32 v151, 0xffff0000, v63
	v_pk_mul_f32 v[150:151], v[150:151], v[146:147] op_sel_hi:[1,0]
	v_cvt_pk_f16_f32 v63, v150, v151
	s_nop 1
	v_mfma_f32_16x16x32_f16 v[124:127], v[56:59], v[88:91], 0
	v_mfma_f32_16x16x32_f16 v[124:127], v[60:63], v[92:95], v[124:127]
	s_cmp_eq_u32 s6, 0
	s_cbranch_scc1 .Lsc_V_zver_t6
	v_max_f32_e32 v144, 0x0da24260, v20
	v_max_f32_e32 v145, 0x0da24260, v21
	v_max_f32_e32 v156, 0x0da24260, v22
	v_max_f32_e32 v157, 0x0da24260, v23
	v_rcp_f32_e32 v144, v144
	v_rcp_f32_e32 v145, v145
	v_rcp_f32_e32 v156, v156
	v_rcp_f32_e32 v157, v157
	v_pk_mul_f32 v[144:145], v[16:17], v[144:145]
	v_pk_mul_f32 v[156:157], v[18:19], v[156:157]
	v_cvt_pk_f16_f32 v152, v144, v145
	v_cvt_pk_f16_f32 v153, v156, v157
	global_store_dwordx2 v7, v[152:153], s[12:13]
	v_pk_fma_f32 v[16:17], v[96:97], v[112:113], v[16:17]
	v_pk_fma_f32 v[18:19], v[98:99], v[114:115], v[18:19]
	v_pk_add_f32 v[20:21], v[20:21], v[96:97]
	v_pk_add_f32 v[22:23], v[22:23], v[98:99]
	v_max_f32_e32 v144, 0x0da24260, v20
	v_max_f32_e32 v145, 0x0da24260, v21
	v_max_f32_e32 v156, 0x0da24260, v22
	v_max_f32_e32 v157, 0x0da24260, v23
	v_rcp_f32_e32 v144, v144
	v_rcp_f32_e32 v145, v145
	v_rcp_f32_e32 v156, v156
	v_rcp_f32_e32 v157, v157
	v_pk_mul_f32 v[144:145], v[16:17], v[144:145]
	v_pk_mul_f32 v[156:157], v[18:19], v[156:157]
	v_cvt_pk_f16_f32 v154, v144, v145
	v_cvt_pk_f16_f32 v155, v156, v157
	global_store_dwordx2 v160, v[154:155], s[12:13]
	v_pk_fma_f32 v[16:17], v[100:101], v[116:117], v[16:17]
	v_pk_fma_f32 v[18:19], v[102:103], v[118:119], v[18:19]
	v_pk_add_f32 v[20:21], v[20:21], v[100:101]
	v_pk_add_f32 v[22:23], v[22:23], v[102:103]
	v_max_f32_e32 v144, 0x0da24260, v20
	v_max_f32_e32 v145, 0x0da24260, v21
	v_max_f32_e32 v156, 0x0da24260, v22
	v_max_f32_e32 v157, 0x0da24260, v23
	v_rcp_f32_e32 v144, v144
	v_rcp_f32_e32 v145, v145
	v_rcp_f32_e32 v156, v156
	v_rcp_f32_e32 v157, v157
	v_pk_mul_f32 v[144:145], v[16:17], v[144:145]
	v_pk_mul_f32 v[156:157], v[18:19], v[156:157]
	v_cvt_pk_f16_f32 v152, v144, v145
	v_cvt_pk_f16_f32 v153, v156, v157
	global_store_dwordx2 v161, v[152:153], s[12:13]
	v_pk_fma_f32 v[16:17], v[104:105], v[120:121], v[16:17]
	v_pk_fma_f32 v[18:19], v[106:107], v[122:123], v[18:19]
	v_pk_add_f32 v[20:21], v[20:21], v[104:105]
	v_pk_add_f32 v[22:23], v[22:23], v[106:107]
	v_max_f32_e32 v144, 0x0da24260, v20
	v_max_f32_e32 v145, 0x0da24260, v21
	v_max_f32_e32 v156, 0x0da24260, v22
	v_max_f32_e32 v157, 0x0da24260, v23
	v_rcp_f32_e32 v144, v144
	v_rcp_f32_e32 v145, v145
	v_rcp_f32_e32 v156, v156
	v_rcp_f32_e32 v157, v157
	v_pk_mul_f32 v[144:145], v[16:17], v[144:145]
	v_pk_mul_f32 v[156:157], v[18:19], v[156:157]
	v_cvt_pk_f16_f32 v154, v144, v145
	v_cvt_pk_f16_f32 v155, v156, v157
	global_store_dwordx2 v162, v[154:155], s[12:13]
	v_pk_fma_f32 v[16:17], v[108:109], v[124:125], v[16:17]
	v_pk_fma_f32 v[18:19], v[110:111], v[126:127], v[18:19]
	v_pk_add_f32 v[20:21], v[20:21], v[108:109]
	v_pk_add_f32 v[22:23], v[22:23], v[110:111]
	s_add_u32 s12, s12, 0x20000
	s_addc_u32 s13, s13, 0
	s_add_u32 s14, s14, 0x800
	s_addc_u32 s15, s15, 0
	s_branch .Lsc_V_seqdone_t6

.Lsc_V_seqdone_t6:
	s_mov_b32 s17, 122880
	s_waitcnt vmcnt(12)
	s_barrier
	v_add_u32_e32 v140, s17, v3
	v_add_u32_e32 v141, s17, v4
	v_add_u32_e32 v142, s17, v5
	v_add_u32_e32 v143, s17, v6
	ds_read_b128 v[32:35], v140 offset:0
	ds_read_b128 v[36:39], v141 offset:0
	ds_read_b128 v[64:67], v142 offset:0
	ds_read_b128 v[68:71], v143 offset:0
	ds_read_b128 v[40:43], v140 offset:8192
	ds_read_b128 v[44:47], v141 offset:8192
	ds_read_b128 v[72:75], v142 offset:2048
	ds_read_b128 v[76:79], v143 offset:2048
	ds_read_b128 v[48:51], v140 offset:16384
	ds_read_b128 v[52:55], v141 offset:16384
	ds_read_b128 v[80:83], v142 offset:4096
	ds_read_b128 v[84:87], v143 offset:4096
	ds_read_b128 v[56:59], v140 offset:24576
	ds_read_b128 v[60:63], v141 offset:24576
	ds_read_b128 v[88:91], v142 offset:6144
	ds_read_b128 v[92:95], v143 offset:6144
	s_waitcnt lgkmcnt(8)
	v_mfma_f32_16x16x32_bf16 v[128:131], v[10:13], v[32:35], 0
	v_mfma_f32_16x16x32_bf16 v[96:99], v[32:35], v[10:13], 0
	v_mfma_f32_16x16x32_bf16 v[128:131], v[10:13], v[36:39], v[128:131]
	v_mfma_f32_16x16x32_bf16 v[96:99], v[36:39], v[10:13], v[96:99]
	v_mfma_f32_16x16x32_bf16 v[132:135], v[10:13], v[40:43], 0
	v_mfma_f32_16x16x32_bf16 v[100:103], v[40:43], v[10:13], 0
	v_mfma_f32_16x16x32_bf16 v[132:135], v[10:13], v[44:47], v[132:135]
	v_mfma_f32_16x16x32_bf16 v[100:103], v[44:47], v[10:13], v[100:103]
	s_waitcnt lgkmcnt(4)
	v_mfma_f32_16x16x32_bf16 v[136:139], v[10:13], v[48:51], 0
	v_mfma_f32_16x16x32_bf16 v[104:107], v[48:51], v[10:13], 0
	v_mfma_f32_16x16x32_bf16 v[136:139], v[10:13], v[52:55], v[136:139]
	v_mfma_f32_16x16x32_bf16 v[104:107], v[52:55], v[10:13], v[104:107]
	s_waitcnt lgkmcnt(0)
	v_mfma_f32_16x16x32_bf16 v[140:143], v[10:13], v[56:59], 0
	v_mfma_f32_16x16x32_bf16 v[108:111], v[56:59], v[10:13], 0
	v_mfma_f32_16x16x32_bf16 v[140:143], v[10:13], v[60:63], v[140:143]
	v_mfma_f32_16x16x32_bf16 v[108:111], v[60:63], v[10:13], v[108:111]
	v_rcp_f32_e32 v146, v128
	v_lshlrev_b32_e32 v148, 16, v32
	v_and_b32_e32 v149, 0xffff0000, v32
	v_pk_mul_f32 v[148:149], v[148:149], v[146:147] op_sel_hi:[1,0]
	v_cvt_pk_f16_f32 v32, v148, v149
	v_lshlrev_b32_e32 v150, 16, v33
	v_and_b32_e32 v151, 0xffff0000, v33
	v_pk_mul_f32 v[150:151], v[150:151], v[146:147] op_sel_hi:[1,0]
	v_cvt_pk_f16_f32 v33, v150, v151
	v_lshlrev_b32_e32 v148, 16, v34
	v_and_b32_e32 v149, 0xffff0000, v34
	v_pk_mul_f32 v[148:149], v[148:149], v[146:147] op_sel_hi:[1,0]
	v_cvt_pk_f16_f32 v34, v148, v149
	v_lshlrev_b32_e32 v150, 16, v35
	v_and_b32_e32 v151, 0xffff0000, v35
	v_pk_mul_f32 v[150:151], v[150:151], v[146:147] op_sel_hi:[1,0]
	v_cvt_pk_f16_f32 v35, v150, v151
	v_lshlrev_b32_e32 v148, 16, v36
	v_and_b32_e32 v149, 0xffff0000, v36
	v_pk_mul_f32 v[148:149], v[148:149], v[146:147] op_sel_hi:[1,0]
	v_cvt_pk_f16_f32 v36, v148, v149
	v_lshlrev_b32_e32 v150, 16, v37
	v_and_b32_e32 v151, 0xffff0000, v37
	v_pk_mul_f32 v[150:151], v[150:151], v[146:147] op_sel_hi:[1,0]
	v_cvt_pk_f16_f32 v37, v150, v151
	v_lshlrev_b32_e32 v148, 16, v38
	v_and_b32_e32 v149, 0xffff0000, v38
	v_pk_mul_f32 v[148:149], v[148:149], v[146:147] op_sel_hi:[1,0]
	v_cvt_pk_f16_f32 v38, v148, v149
	v_lshlrev_b32_e32 v150, 16, v39
	v_and_b32_e32 v151, 0xffff0000, v39
	v_pk_mul_f32 v[150:151], v[150:151], v[146:147] op_sel_hi:[1,0]
	v_cvt_pk_f16_f32 v39, v150, v151
	s_nop 1
	v_mfma_f32_16x16x32_f16 v[112:115], v[32:35], v[64:67], 0
	v_mfma_f32_16x16x32_f16 v[112:115], v[36:39], v[68:71], v[112:115]
	v_rcp_f32_e32 v146, v132
	v_lshlrev_b32_e32 v148, 16, v40
	v_and_b32_e32 v149, 0xffff0000, v40
	v_pk_mul_f32 v[148:149], v[148:149], v[146:147] op_sel_hi:[1,0]
	v_cvt_pk_f16_f32 v40, v148, v149
	v_lshlrev_b32_e32 v150, 16, v41
	v_and_b32_e32 v151, 0xffff0000, v41
	v_pk_mul_f32 v[150:151], v[150:151], v[146:147] op_sel_hi:[1,0]
	v_cvt_pk_f16_f32 v41, v150, v151
	v_lshlrev_b32_e32 v148, 16, v42
	v_and_b32_e32 v149, 0xffff0000, v42
	v_pk_mul_f32 v[148:149], v[148:149], v[146:147] op_sel_hi:[1,0]
	v_cvt_pk_f16_f32 v42, v148, v149
	v_lshlrev_b32_e32 v150, 16, v43
	v_and_b32_e32 v151, 0xffff0000, v43
	v_pk_mul_f32 v[150:151], v[150:151], v[146:147] op_sel_hi:[1,0]
	v_cvt_pk_f16_f32 v43, v150, v151
	v_lshlrev_b32_e32 v148, 16, v44
	v_and_b32_e32 v149, 0xffff0000, v44
	v_pk_mul_f32 v[148:149], v[148:149], v[146:147] op_sel_hi:[1,0]
	v_cvt_pk_f16_f32 v44, v148, v149
	v_lshlrev_b32_e32 v150, 16, v45
	v_and_b32_e32 v151, 0xffff0000, v45
	v_pk_mul_f32 v[150:151], v[150:151], v[146:147] op_sel_hi:[1,0]
	v_cvt_pk_f16_f32 v45, v150, v151
	v_lshlrev_b32_e32 v148, 16, v46
	v_and_b32_e32 v149, 0xffff0000, v46
	v_pk_mul_f32 v[148:149], v[148:149], v[146:147] op_sel_hi:[1,0]
	v_cvt_pk_f16_f32 v46, v148, v149
	v_lshlrev_b32_e32 v150, 16, v47
	v_and_b32_e32 v151, 0xffff0000, v47
	v_pk_mul_f32 v[150:151], v[150:151], v[146:147] op_sel_hi:[1,0]
	v_cvt_pk_f16_f32 v47, v150, v151
	s_nop 1
	v_mfma_f32_16x16x32_f16 v[116:119], v[40:43], v[72:75], 0
	v_mfma_f32_16x16x32_f16 v[116:119], v[44:47], v[76:79], v[116:119]
	v_rcp_f32_e32 v146, v136
	v_lshlrev_b32_e32 v148, 16, v48
	v_and_b32_e32 v149, 0xffff0000, v48
	v_pk_mul_f32 v[148:149], v[148:149], v[146:147] op_sel_hi:[1,0]
	v_cvt_pk_f16_f32 v48, v148, v149
	v_lshlrev_b32_e32 v150, 16, v49
	v_and_b32_e32 v151, 0xffff0000, v49
	v_pk_mul_f32 v[150:151], v[150:151], v[146:147] op_sel_hi:[1,0]
	v_cvt_pk_f16_f32 v49, v150, v151
	v_lshlrev_b32_e32 v148, 16, v50
	v_and_b32_e32 v149, 0xffff0000, v50
	v_pk_mul_f32 v[148:149], v[148:149], v[146:147] op_sel_hi:[1,0]
	v_cvt_pk_f16_f32 v50, v148, v149
	v_lshlrev_b32_e32 v150, 16, v51
	v_and_b32_e32 v151, 0xffff0000, v51
	v_pk_mul_f32 v[150:151], v[150:151], v[146:147] op_sel_hi:[1,0]
	v_cvt_pk_f16_f32 v51, v150, v151
	v_lshlrev_b32_e32 v148, 16, v52
	v_and_b32_e32 v149, 0xffff0000, v52
	v_pk_mul_f32 v[148:149], v[148:149], v[146:147] op_sel_hi:[1,0]
	v_cvt_pk_f16_f32 v52, v148, v149
	v_lshlrev_b32_e32 v150, 16, v53
	v_and_b32_e32 v151, 0xffff0000, v53
	v_pk_mul_f32 v[150:151], v[150:151], v[146:147] op_sel_hi:[1,0]
	v_cvt_pk_f16_f32 v53, v150, v151
	v_lshlrev_b32_e32 v148, 16, v54
	v_and_b32_e32 v149, 0xffff0000, v54
	v_pk_mul_f32 v[148:149], v[148:149], v[146:147] op_sel_hi:[1,0]
	v_cvt_pk_f16_f32 v54, v148, v149
	v_lshlrev_b32_e32 v150, 16, v55
	v_and_b32_e32 v151, 0xffff0000, v55
	v_pk_mul_f32 v[150:151], v[150:151], v[146:147] op_sel_hi:[1,0]
	v_cvt_pk_f16_f32 v55, v150, v151
	s_nop 1
	v_mfma_f32_16x16x32_f16 v[120:123], v[48:51], v[80:83], 0
	v_mfma_f32_16x16x32_f16 v[120:123], v[52:55], v[84:87], v[120:123]
	v_rcp_f32_e32 v146, v140
	v_lshlrev_b32_e32 v148, 16, v56
	v_and_b32_e32 v149, 0xffff0000, v56
	v_pk_mul_f32 v[148:149], v[148:149], v[146:147] op_sel_hi:[1,0]
	v_cvt_pk_f16_f32 v56, v148, v149
	v_lshlrev_b32_e32 v150, 16, v57
	v_and_b32_e32 v151, 0xffff0000, v57
	v_pk_mul_f32 v[150:151], v[150:151], v[146:147] op_sel_hi:[1,0]
	v_cvt_pk_f16_f32 v57, v150, v151
	v_lshlrev_b32_e32 v148, 16, v58
	v_and_b32_e32 v149, 0xffff0000, v58
	v_pk_mul_f32 v[148:149], v[148:149], v[146:147] op_sel_hi:[1,0]
	v_cvt_pk_f16_f32 v58, v148, v149
	v_lshlrev_b32_e32 v150, 16, v59
	v_and_b32_e32 v151, 0xffff0000, v59
	v_pk_mul_f32 v[150:151], v[150:151], v[146:147] op_sel_hi:[1,0]
	v_cvt_pk_f16_f32 v59, v150, v151
	v_lshlrev_b32_e32 v148, 16, v60
	v_and_b32_e32 v149, 0xffff0000, v60
	v_pk_mul_f32 v[148:149], v[148:149], v[146:147] op_sel_hi:[1,0]
	v_cvt_pk_f16_f32 v60, v148, v149
	v_lshlrev_b32_e32 v150, 16, v61
	v_and_b32_e32 v151, 0xffff0000, v61
	v_pk_mul_f32 v[150:151], v[150:151], v[146:147] op_sel_hi:[1,0]
	v_cvt_pk_f16_f32 v61, v150, v151
	v_lshlrev_b32_e32 v148, 16, v62
	v_and_b32_e32 v149, 0xffff0000, v62
	v_pk_mul_f32 v[148:149], v[148:149], v[146:147] op_sel_hi:[1,0]
	v_cvt_pk_f16_f32 v62, v148, v149
	v_lshlrev_b32_e32 v150, 16, v63
	v_and_b32_e32 v151, 0xffff0000, v63
	v_pk_mul_f32 v[150:151], v[150:151], v[146:147] op_sel_hi:[1,0]
	v_cvt_pk_f16_f32 v63, v150, v151
	s_nop 1
	v_mfma_f32_16x16x32_f16 v[124:127], v[56:59], v[88:91], 0
	v_mfma_f32_16x16x32_f16 v[124:127], v[60:63], v[92:95], v[124:127]
	s_cmp_eq_u32 s6, 0
	s_cbranch_scc1 .Lsc_V_zver_t7
	v_max_f32_e32 v144, 0x0da24260, v20
	v_max_f32_e32 v145, 0x0da24260, v21
	v_max_f32_e32 v156, 0x0da24260, v22
	v_max_f32_e32 v157, 0x0da24260, v23
	v_rcp_f32_e32 v144, v144
	v_rcp_f32_e32 v145, v145
	v_rcp_f32_e32 v156, v156
	v_rcp_f32_e32 v157, v157
	v_pk_mul_f32 v[144:145], v[16:17], v[144:145]
	v_pk_mul_f32 v[156:157], v[18:19], v[156:157]
	v_cvt_pk_f16_f32 v152, v144, v145
	v_cvt_pk_f16_f32 v153, v156, v157
	global_store_dwordx2 v7, v[152:153], s[12:13]
	v_pk_fma_f32 v[16:17], v[96:97], v[112:113], v[16:17]
	v_pk_fma_f32 v[18:19], v[98:99], v[114:115], v[18:19]
	v_pk_add_f32 v[20:21], v[20:21], v[96:97]
	v_pk_add_f32 v[22:23], v[22:23], v[98:99]
	v_max_f32_e32 v144, 0x0da24260, v20
	v_max_f32_e32 v145, 0x0da24260, v21
	v_max_f32_e32 v156, 0x0da24260, v22
	v_max_f32_e32 v157, 0x0da24260, v23
	v_rcp_f32_e32 v144, v144
	v_rcp_f32_e32 v145, v145
	v_rcp_f32_e32 v156, v156
	v_rcp_f32_e32 v157, v157
	v_pk_mul_f32 v[144:145], v[16:17], v[144:145]
	v_pk_mul_f32 v[156:157], v[18:19], v[156:157]
	v_cvt_pk_f16_f32 v154, v144, v145
	v_cvt_pk_f16_f32 v155, v156, v157
	global_store_dwordx2 v160, v[154:155], s[12:13]
	v_pk_fma_f32 v[16:17], v[100:101], v[116:117], v[16:17]
	v_pk_fma_f32 v[18:19], v[102:103], v[118:119], v[18:19]
	v_pk_add_f32 v[20:21], v[20:21], v[100:101]
	v_pk_add_f32 v[22:23], v[22:23], v[102:103]
	v_max_f32_e32 v144, 0x0da24260, v20
	v_max_f32_e32 v145, 0x0da24260, v21
	v_max_f32_e32 v156, 0x0da24260, v22
	v_max_f32_e32 v157, 0x0da24260, v23
	v_rcp_f32_e32 v144, v144
	v_rcp_f32_e32 v145, v145
	v_rcp_f32_e32 v156, v156
	v_rcp_f32_e32 v157, v157
	v_pk_mul_f32 v[144:145], v[16:17], v[144:145]
	v_pk_mul_f32 v[156:157], v[18:19], v[156:157]
	v_cvt_pk_f16_f32 v152, v144, v145
	v_cvt_pk_f16_f32 v153, v156, v157
	global_store_dwordx2 v161, v[152:153], s[12:13]
	v_pk_fma_f32 v[16:17], v[104:105], v[120:121], v[16:17]
	v_pk_fma_f32 v[18:19], v[106:107], v[122:123], v[18:19]
	v_pk_add_f32 v[20:21], v[20:21], v[104:105]
	v_pk_add_f32 v[22:23], v[22:23], v[106:107]
	v_max_f32_e32 v144, 0x0da24260, v20
	v_max_f32_e32 v145, 0x0da24260, v21
	v_max_f32_e32 v156, 0x0da24260, v22
	v_max_f32_e32 v157, 0x0da24260, v23
	v_rcp_f32_e32 v144, v144
	v_rcp_f32_e32 v145, v145
	v_rcp_f32_e32 v156, v156
	v_rcp_f32_e32 v157, v157
	v_pk_mul_f32 v[144:145], v[16:17], v[144:145]
	v_pk_mul_f32 v[156:157], v[18:19], v[156:157]
	v_cvt_pk_f16_f32 v154, v144, v145
	v_cvt_pk_f16_f32 v155, v156, v157
	global_store_dwordx2 v162, v[154:155], s[12:13]
	v_pk_fma_f32 v[16:17], v[108:109], v[124:125], v[16:17]
	v_pk_fma_f32 v[18:19], v[110:111], v[126:127], v[18:19]
	v_pk_add_f32 v[20:21], v[20:21], v[108:109]
	v_pk_add_f32 v[22:23], v[22:23], v[110:111]
	s_add_u32 s12, s12, 0x20000
	s_addc_u32 s13, s13, 0
	s_add_u32 s14, s14, 0x800
	s_addc_u32 s15, s15, 0
	s_branch .Lsc_V_seqdone_t7

.Lsc_K_setup:
	v_bfe_u32 v30, v0, 1, 6
	v_lshlrev_b32_e32 v30, 9, v30
	v_and_b32_e32 v31, 1, v0
	v_lshlrev_b32_e32 v31, 4, v31
	v_or3_b32 v2, v29, v30, v31
	v_lshrrev_b32_e32 v30, 2, v15
	v_lshl_add_u32 v30, v25, 3, v30
	v_and_b32_e32 v31, 3, v15
	v_lshlrev_b32_e32 v31, 3, v31
	v_lshl_or_b32 v5, v30, 5, v31
	v_add_u32_e32 v5, 0x8000, v5
	v_lshlrev_b32_e32 v7, 9, v15
	v_lshl_add_u32 v7, v25, 3, v7
	s_lshl_b32 s44, s7, 13
	s_lshl_b32 s45, s6, 5
	s_add_u32 s44, s44, s45
	v_add_u32_e32 v7, s44, v7
	v_lshlrev_b32_e32 v8, 4, v25
	s_lshl_b32 s44, s7, 6
	v_add_u32_e32 v8, s44, v8
	s_add_u32 s8, s28, s42
	s_addc_u32 s9, s29, 0
	s_lshl_b32 s44, s6, 5
	s_add_u32 s44, s44, s43
	s_add_u32 s10, s24, s44
	s_addc_u32 s11, s25, 0
	s_add_u32 s12, s36, s43
	s_addc_u32 s13, s37, 0
	v_add_u32_e32 v160, 0x8000, v7
	v_add_u32_e32 v161, 0x10000, v7
	v_add_u32_e32 v162, 0x18000, v7
	s_add_u32 s18, s19, 0
	s_mov_b32 m0, s18
	s_mov_b64 s[46:47], s[8:9]
	global_load_lds_dwordx4 v1, s[46:47]
	s_add_u32 m0, m0, 0x1000
	s_add_u32 s46, s46, 0x1000
	s_addc_u32 s47, s47, 0
	global_load_lds_dwordx4 v1, s[46:47]
	s_add_u32 m0, m0, 0x1000
	s_add_u32 s46, s46, 0x1000
	s_addc_u32 s47, s47, 0
	global_load_lds_dwordx4 v1, s[46:47]
	s_add_u32 m0, m0, 0x1000
	s_add_u32 s46, s46, 0x1000
	s_addc_u32 s47, s47, 0
	global_load_lds_dwordx4 v1, s[46:47]
	s_add_u32 m0, m0, 0x1000
	s_add_u32 s46, s46, 0x1000
	s_addc_u32 s47, s47, 0
	global_load_lds_dwordx4 v1, s[46:47]
	s_add_u32 m0, m0, 0x1000
	s_add_u32 s46, s46, 0x1000
	s_addc_u32 s47, s47, 0
	global_load_lds_dwordx4 v1, s[46:47]
	s_add_u32 m0, m0, 0x1000
	s_add_u32 s46, s46, 0x1000
	s_addc_u32 s47, s47, 0
	global_load_lds_dwordx4 v1, s[46:47]
	s_add_u32 m0, m0, 0x1000
	s_add_u32 s46, s46, 0x1000
	s_addc_u32 s47, s47, 0
	global_load_lds_dwordx4 v1, s[46:47]
	s_add_u32 m0, m0, 0x1000
	s_mov_b64 s[46:47], s[10:11]
	s_nop 0
	global_load_lds_dwordx4 v2, s[46:47]
	s_add_u32 m0, m0, 0x1000
	s_add_u32 s46, s46, 0x10000
	s_addc_u32 s47, s47, 0
	global_load_lds_dwordx4 v2, s[46:47]
	s_add_u32 s8, s8, 0x8000
	s_addc_u32 s9, s9, 0
	s_add_u32 s10, s10, 0x20000
	s_addc_u32 s11, s11, 0
	s_add_u32 s18, s19, 40960
	s_mov_b32 m0, s18
	s_mov_b64 s[46:47], s[8:9]
	global_load_lds_dwordx4 v1, s[46:47]
	s_add_u32 m0, m0, 0x1000
	s_add_u32 s46, s46, 0x1000
	s_addc_u32 s47, s47, 0
	global_load_lds_dwordx4 v1, s[46:47]
	s_add_u32 m0, m0, 0x1000
	s_add_u32 s46, s46, 0x1000
	s_addc_u32 s47, s47, 0
	global_load_lds_dwordx4 v1, s[46:47]
	s_add_u32 m0, m0, 0x1000
	s_add_u32 s46, s46, 0x1000
	s_addc_u32 s47, s47, 0
	global_load_lds_dwordx4 v1, s[46:47]
	s_add_u32 m0, m0, 0x1000
	s_add_u32 s46, s46, 0x1000
	s_addc_u32 s47, s47, 0
	global_load_lds_dwordx4 v1, s[46:47]
	s_add_u32 m0, m0, 0x1000
	s_add_u32 s46, s46, 0x1000
	s_addc_u32 s47, s47, 0
	global_load_lds_dwordx4 v1, s[46:47]
	s_add_u32 m0, m0, 0x1000
	s_add_u32 s46, s46, 0x1000
	s_addc_u32 s47, s47, 0
	global_load_lds_dwordx4 v1, s[46:47]
	s_add_u32 m0, m0, 0x1000
	s_add_u32 s46, s46, 0x1000
	s_addc_u32 s47, s47, 0
	global_load_lds_dwordx4 v1, s[46:47]
	s_add_u32 m0, m0, 0x1000
	s_mov_b64 s[46:47], s[10:11]
	s_nop 0
	global_load_lds_dwordx4 v2, s[46:47]
	s_add_u32 m0, m0, 0x1000
	s_add_u32 s46, s46, 0x10000
	s_addc_u32 s47, s47, 0
	global_load_lds_dwordx4 v2, s[46:47]
	s_add_u32 s8, s8, 0x8000
	s_addc_u32 s9, s9, 0
	s_add_u32 s10, s10, 0x20000
	s_addc_u32 s11, s11, 0
	s_add_u32 s18, s19, 81920
	s_mov_b32 m0, s18
	s_mov_b64 s[46:47], s[8:9]
	global_load_lds_dwordx4 v1, s[46:47]
	s_add_u32 m0, m0, 0x1000
	s_add_u32 s46, s46, 0x1000
	s_addc_u32 s47, s47, 0
	global_load_lds_dwordx4 v1, s[46:47]
	s_add_u32 m0, m0, 0x1000
	s_add_u32 s46, s46, 0x1000
	s_addc_u32 s47, s47, 0
	global_load_lds_dwordx4 v1, s[46:47]
	s_add_u32 m0, m0, 0x1000
	s_add_u32 s46, s46, 0x1000
	s_addc_u32 s47, s47, 0
	global_load_lds_dwordx4 v1, s[46:47]
	s_add_u32 m0, m0, 0x1000
	s_add_u32 s46, s46, 0x1000
	s_addc_u32 s47, s47, 0
	global_load_lds_dwordx4 v1, s[46:47]
	s_add_u32 m0, m0, 0x1000
	s_add_u32 s46, s46, 0x1000
	s_addc_u32 s47, s47, 0
	global_load_lds_dwordx4 v1, s[46:47]
	s_add_u32 m0, m0, 0x1000
	s_add_u32 s46, s46, 0x1000
	s_addc_u32 s47, s47, 0
	global_load_lds_dwordx4 v1, s[46:47]
	s_add_u32 m0, m0, 0x1000
	s_add_u32 s46, s46, 0x1000
	s_addc_u32 s47, s47, 0
	global_load_lds_dwordx4 v1, s[46:47]
	s_add_u32 m0, m0, 0x1000
	s_mov_b64 s[46:47], s[10:11]
	s_nop 0
	global_load_lds_dwordx4 v2, s[46:47]
	s_add_u32 m0, m0, 0x1000
	s_add_u32 s46, s46, 0x10000
	s_addc_u32 s47, s47, 0
	global_load_lds_dwordx4 v2, s[46:47]
	s_add_u32 s8, s8, 0x8000
	s_addc_u32 s9, s9, 0
	s_add_u32 s10, s10, 0x20000
	s_addc_u32 s11, s11, 0
	s_add_u32 s18, s19, 122880

.Lsc_K_wd:
	s_barrier
	v_add_u32_e32 v140, s17, v3
	v_add_u32_e32 v141, s17, v4
	v_add_u32_e32 v142, s17, v5
	ds_read_b128 v[32:35], v140 offset:0
	ds_read_b128 v[36:39], v141 offset:0
	ds_read_b64_tr_b16 v[64:65], v142 offset:0
	ds_read_b64_tr_b16 v[66:67], v142 offset:128
	ds_read_b64_tr_b16 v[68:69], v142 offset:1024
	ds_read_b64_tr_b16 v[70:71], v142 offset:1152
	ds_read_b128 v[40:43], v140 offset:8192
	ds_read_b128 v[44:47], v141 offset:8192
	ds_read_b64_tr_b16 v[72:73], v142 offset:2048
	ds_read_b64_tr_b16 v[74:75], v142 offset:2176
	ds_read_b64_tr_b16 v[76:77], v142 offset:3072
	ds_read_b64_tr_b16 v[78:79], v142 offset:3200
	ds_read_b128 v[48:51], v140 offset:16384
	ds_read_b128 v[52:55], v141 offset:16384
	ds_read_b64_tr_b16 v[80:81], v142 offset:4096
	ds_read_b64_tr_b16 v[82:83], v142 offset:4224
	ds_read_b64_tr_b16 v[84:85], v142 offset:5120
	ds_read_b64_tr_b16 v[86:87], v142 offset:5248
	ds_read_b128 v[56:59], v140 offset:24576
	ds_read_b128 v[60:63], v141 offset:24576
	ds_read_b64_tr_b16 v[88:89], v142 offset:6144
	ds_read_b64_tr_b16 v[90:91], v142 offset:6272
	ds_read_b64_tr_b16 v[92:93], v142 offset:7168
	ds_read_b64_tr_b16 v[94:95], v142 offset:7296
	s_mov_b32 m0, s18
	s_mov_b64 s[46:47], s[8:9]
	global_load_lds_dwordx4 v1, s[46:47]
	s_add_u32 m0, m0, 0x1000
	s_add_u32 s46, s46, 0x1000
	s_addc_u32 s47, s47, 0
	global_load_lds_dwordx4 v1, s[46:47]
	s_add_u32 m0, m0, 0x1000
	s_add_u32 s46, s46, 0x1000
	s_addc_u32 s47, s47, 0
	global_load_lds_dwordx4 v1, s[46:47]
	s_add_u32 m0, m0, 0x1000
	s_add_u32 s46, s46, 0x1000
	s_addc_u32 s47, s47, 0
	global_load_lds_dwordx4 v1, s[46:47]
	s_add_u32 m0, m0, 0x1000
	s_add_u32 s46, s46, 0x1000
	s_addc_u32 s47, s47, 0
	global_load_lds_dwordx4 v1, s[46:47]
	s_add_u32 m0, m0, 0x1000
	s_add_u32 s46, s46, 0x1000
	s_addc_u32 s47, s47, 0
	global_load_lds_dwordx4 v1, s[46:47]
	s_add_u32 m0, m0, 0x1000
	s_add_u32 s46, s46, 0x1000
	s_addc_u32 s47, s47, 0
	global_load_lds_dwordx4 v1, s[46:47]
	s_add_u32 m0, m0, 0x1000
	s_add_u32 s46, s46, 0x1000
	s_addc_u32 s47, s47, 0
	global_load_lds_dwordx4 v1, s[46:47]
	s_add_u32 m0, m0, 0x1000
	s_mov_b64 s[46:47], s[10:11]
	s_nop 0
	global_load_lds_dwordx4 v2, s[46:47]
	s_add_u32 m0, m0, 0x1000
	s_add_u32 s46, s46, 0x10000
	s_addc_u32 s47, s47, 0
	global_load_lds_dwordx4 v2, s[46:47]
	s_add_u32 s8, s8, 0x8000
	s_addc_u32 s9, s9, 0
	s_add_u32 s10, s10, 0x20000
	s_addc_u32 s11, s11, 0
	s_waitcnt lgkmcnt(12)
	v_mfma_f32_16x16x32_bf16 v[96:99], v[32:35], v[10:13], 0
	v_mfma_f32_16x16x32_bf16 v[112:115], v[64:67], v[32:35], 0
	v_mfma_f32_16x16x32_bf16 v[96:99], v[36:39], v[10:13], v[96:99]
	v_mfma_f32_16x16x32_bf16 v[112:115], v[68:71], v[36:39], v[112:115]
	v_mfma_f32_16x16x32_bf16 v[100:103], v[40:43], v[10:13], 0
	v_mfma_f32_16x16x32_bf16 v[116:119], v[72:75], v[40:43], 0
	v_mfma_f32_16x16x32_bf16 v[100:103], v[44:47], v[10:13], v[100:103]
	v_mfma_f32_16x16x32_bf16 v[116:119], v[76:79], v[44:47], v[116:119]
	s_waitcnt lgkmcnt(6)
	v_mfma_f32_16x16x32_bf16 v[104:107], v[48:51], v[10:13], 0
	v_mfma_f32_16x16x32_bf16 v[120:123], v[80:83], v[48:51], 0
	v_mfma_f32_16x16x32_bf16 v[104:107], v[52:55], v[10:13], v[104:107]
	v_mfma_f32_16x16x32_bf16 v[120:123], v[84:87], v[52:55], v[120:123]
	s_waitcnt lgkmcnt(0)
	v_mfma_f32_16x16x32_bf16 v[108:111], v[56:59], v[10:13], 0
	v_mfma_f32_16x16x32_bf16 v[124:127], v[88:91], v[56:59], 0
	v_mfma_f32_16x16x32_bf16 v[108:111], v[60:63], v[10:13], v[108:111]
	v_mfma_f32_16x16x32_bf16 v[124:127], v[92:95], v[60:63], v[124:127]
	s_cmp_eq_u32 s6, 0
	s_cbranch_scc1 .Lsc_K_zver_l
	v_cvt_pk_bf16_f32 v152, v16, v17
	v_cvt_pk_bf16_f32 v153, v18, v19
	global_store_dwordx2 v7, v[152:153], s[12:13]
	v_pk_add_f32 v[16:17], v[16:17], v[112:113]
	v_pk_add_f32 v[18:19], v[18:19], v[114:115]
	v_pk_add_f32 v[20:21], v[20:21], v[96:97]
	v_pk_add_f32 v[22:23], v[22:23], v[98:99]
	v_cvt_pk_bf16_f32 v154, v16, v17
	v_cvt_pk_bf16_f32 v155, v18, v19
	global_store_dwordx2 v160, v[154:155], s[12:13]
	v_pk_add_f32 v[16:17], v[16:17], v[116:117]
	v_pk_add_f32 v[18:19], v[18:19], v[118:119]
	v_pk_add_f32 v[20:21], v[20:21], v[100:101]
	v_pk_add_f32 v[22:23], v[22:23], v[102:103]
	v_cvt_pk_bf16_f32 v152, v16, v17
	v_cvt_pk_bf16_f32 v153, v18, v19
	global_store_dwordx2 v161, v[152:153], s[12:13]
	v_pk_add_f32 v[16:17], v[16:17], v[120:121]
	v_pk_add_f32 v[18:19], v[18:19], v[122:123]
	v_pk_add_f32 v[20:21], v[20:21], v[104:105]
	v_pk_add_f32 v[22:23], v[22:23], v[106:107]
	v_cvt_pk_bf16_f32 v154, v16, v17
	v_cvt_pk_bf16_f32 v155, v18, v19
	global_store_dwordx2 v162, v[154:155], s[12:13]
	v_pk_add_f32 v[16:17], v[16:17], v[124:125]
	v_pk_add_f32 v[18:19], v[18:19], v[126:127]
	v_pk_add_f32 v[20:21], v[20:21], v[108:109]
	v_pk_add_f32 v[22:23], v[22:23], v[110:111]
	s_add_u32 s12, s12, 0x20000
	s_addc_u32 s13, s13, 0
	s_add_u32 s14, s14, 0x800
	s_addc_u32 s15, s15, 0
	s_branch .Lsc_K_seqdone_l
.Lsc_K_zver_l:
	v_cvt_pk_bf16_f32 v152, v16, v17
	v_cvt_pk_bf16_f32 v153, v18, v19
	global_store_dwordx2 v7, v[152:153], s[12:13]
	s_mov_b64 exec, s[20:21]
	global_store_dwordx4 v8, v[20:23], s[14:15]
	s_mov_b64 exec, -1
	v_pk_add_f32 v[16:17], v[16:17], v[112:113]
	v_pk_add_f32 v[18:19], v[18:19], v[114:115]
	v_pk_add_f32 v[20:21], v[20:21], v[96:97]
	v_pk_add_f32 v[22:23], v[22:23], v[98:99]
	v_cvt_pk_bf16_f32 v154, v16, v17
	v_cvt_pk_bf16_f32 v155, v18, v19
	global_store_dwordx2 v160, v[154:155], s[12:13]
	s_mov_b64 exec, s[20:21]
	global_store_dwordx4 v8, v[20:23], s[14:15] offset:512
	s_mov_b64 exec, -1
	v_pk_add_f32 v[16:17], v[16:17], v[116:117]
	v_pk_add_f32 v[18:19], v[18:19], v[118:119]
	v_pk_add_f32 v[20:21], v[20:21], v[100:101]
	v_pk_add_f32 v[22:23], v[22:23], v[102:103]
	v_cvt_pk_bf16_f32 v152, v16, v17
	v_cvt_pk_bf16_f32 v153, v18, v19
	global_store_dwordx2 v161, v[152:153], s[12:13]
	s_mov_b64 exec, s[20:21]
	global_store_dwordx4 v8, v[20:23], s[14:15] offset:1024
	s_mov_b64 exec, -1
	v_pk_add_f32 v[16:17], v[16:17], v[120:121]
	v_pk_add_f32 v[18:19], v[18:19], v[122:123]
	v_pk_add_f32 v[20:21], v[20:21], v[104:105]
	v_pk_add_f32 v[22:23], v[22:23], v[106:107]
	v_cvt_pk_bf16_f32 v154, v16, v17
	v_cvt_pk_bf16_f32 v155, v18, v19
	global_store_dwordx2 v162, v[154:155], s[12:13]
	s_mov_b64 exec, s[20:21]
	global_store_dwordx4 v8, v[20:23], s[14:15] offset:1536
	s_mov_b64 exec, -1
	v_pk_add_f32 v[16:17], v[16:17], v[124:125]
	v_pk_add_f32 v[18:19], v[18:19], v[126:127]
	v_pk_add_f32 v[20:21], v[20:21], v[108:109]
	v_pk_add_f32 v[22:23], v[22:23], v[110:111]
	s_add_u32 s12, s12, 0x20000
	s_addc_u32 s13, s13, 0
	s_add_u32 s14, s14, 0x800
	s_addc_u32 s15, s15, 0
.Lsc_K_seqdone_l:
	s_add_u32 s16, s16, 1
	s_and_b32 s44, s16, 3
	s_mul_i32 s17, s44, 40960
	s_add_u32 s44, s16, 3
	s_and_b32 s44, s44, 3
	s_mul_i32 s44, s44, 40960
	s_add_u32 s18, s44, s19
	s_cmp_lt_u32 s16, 5
	s_cbranch_scc1 .Lsc_K_loop
	s_mov_b32 s17, 40960
	s_waitcnt vmcnt(32)
	s_barrier
	v_add_u32_e32 v140, s17, v3
	v_add_u32_e32 v141, s17, v4
	v_add_u32_e32 v142, s17, v5
	ds_read_b128 v[32:35], v140 offset:0
	ds_read_b128 v[36:39], v141 offset:0
	ds_read_b64_tr_b16 v[64:65], v142 offset:0
	ds_read_b64_tr_b16 v[66:67], v142 offset:128
	ds_read_b64_tr_b16 v[68:69], v142 offset:1024
	ds_read_b64_tr_b16 v[70:71], v142 offset:1152
	ds_read_b128 v[40:43], v140 offset:8192
	ds_read_b128 v[44:47], v141 offset:8192
	ds_read_b64_tr_b16 v[72:73], v142 offset:2048
	ds_read_b64_tr_b16 v[74:75], v142 offset:2176
	ds_read_b64_tr_b16 v[76:77], v142 offset:3072
	ds_read_b64_tr_b16 v[78:79], v142 offset:3200
	ds_read_b128 v[48:51], v140 offset:16384
	ds_read_b128 v[52:55], v141 offset:16384
	ds_read_b64_tr_b16 v[80:81], v142 offset:4096
	ds_read_b64_tr_b16 v[82:83], v142 offset:4224
	ds_read_b64_tr_b16 v[84:85], v142 offset:5120
	ds_read_b64_tr_b16 v[86:87], v142 offset:5248
	ds_read_b128 v[56:59], v140 offset:24576
	ds_read_b128 v[60:63], v141 offset:24576
	ds_read_b64_tr_b16 v[88:89], v142 offset:6144
	ds_read_b64_tr_b16 v[90:91], v142 offset:6272
	ds_read_b64_tr_b16 v[92:93], v142 offset:7168
	ds_read_b64_tr_b16 v[94:95], v142 offset:7296
	s_waitcnt lgkmcnt(12)
	v_mfma_f32_16x16x32_bf16 v[96:99], v[32:35], v[10:13], 0
	v_mfma_f32_16x16x32_bf16 v[112:115], v[64:67], v[32:35], 0
	v_mfma_f32_16x16x32_bf16 v[96:99], v[36:39], v[10:13], v[96:99]
	v_mfma_f32_16x16x32_bf16 v[112:115], v[68:71], v[36:39], v[112:115]
	v_mfma_f32_16x16x32_bf16 v[100:103], v[40:43], v[10:13], 0
	v_mfma_f32_16x16x32_bf16 v[116:119], v[72:75], v[40:43], 0
	v_mfma_f32_16x16x32_bf16 v[100:103], v[44:47], v[10:13], v[100:103]
	v_mfma_f32_16x16x32_bf16 v[116:119], v[76:79], v[44:47], v[116:119]
	s_waitcnt lgkmcnt(6)
	v_mfma_f32_16x16x32_bf16 v[104:107], v[48:51], v[10:13], 0
	v_mfma_f32_16x16x32_bf16 v[120:123], v[80:83], v[48:51], 0
	v_mfma_f32_16x16x32_bf16 v[104:107], v[52:55], v[10:13], v[104:107]
	v_mfma_f32_16x16x32_bf16 v[120:123], v[84:87], v[52:55], v[120:123]
	s_waitcnt lgkmcnt(0)
	v_mfma_f32_16x16x32_bf16 v[108:111], v[56:59], v[10:13], 0
	v_mfma_f32_16x16x32_bf16 v[124:127], v[88:91], v[56:59], 0
	v_mfma_f32_16x16x32_bf16 v[108:111], v[60:63], v[10:13], v[108:111]
	v_mfma_f32_16x16x32_bf16 v[124:127], v[92:95], v[60:63], v[124:127]
	s_cmp_eq_u32 s6, 0
	s_cbranch_scc1 .Lsc_K_zver_t5
	v_cvt_pk_bf16_f32 v152, v16, v17
	v_cvt_pk_bf16_f32 v153, v18, v19
	global_store_dwordx2 v7, v[152:153], s[12:13]
	v_pk_add_f32 v[16:17], v[16:17], v[112:113]
	v_pk_add_f32 v[18:19], v[18:19], v[114:115]
	v_pk_add_f32 v[20:21], v[20:21], v[96:97]
	v_pk_add_f32 v[22:23], v[22:23], v[98:99]
	v_cvt_pk_bf16_f32 v154, v16, v17
	v_cvt_pk_bf16_f32 v155, v18, v19
	global_store_dwordx2 v160, v[154:155], s[12:13]
	v_pk_add_f32 v[16:17], v[16:17], v[116:117]
	v_pk_add_f32 v[18:19], v[18:19], v[118:119]
	v_pk_add_f32 v[20:21], v[20:21], v[100:101]
	v_pk_add_f32 v[22:23], v[22:23], v[102:103]
	v_cvt_pk_bf16_f32 v152, v16, v17
	v_cvt_pk_bf16_f32 v153, v18, v19
	global_store_dwordx2 v161, v[152:153], s[12:13]
	v_pk_add_f32 v[16:17], v[16:17], v[120:121]
	v_pk_add_f32 v[18:19], v[18:19], v[122:123]
	v_pk_add_f32 v[20:21], v[20:21], v[104:105]
	v_pk_add_f32 v[22:23], v[22:23], v[106:107]
	v_cvt_pk_bf16_f32 v154, v16, v17
	v_cvt_pk_bf16_f32 v155, v18, v19
	global_store_dwordx2 v162, v[154:155], s[12:13]
	v_pk_add_f32 v[16:17], v[16:17], v[124:125]
	v_pk_add_f32 v[18:19], v[18:19], v[126:127]
	v_pk_add_f32 v[20:21], v[20:21], v[108:109]
	v_pk_add_f32 v[22:23], v[22:23], v[110:111]
	s_add_u32 s12, s12, 0x20000
	s_addc_u32 s13, s13, 0
	s_add_u32 s14, s14, 0x800
	s_addc_u32 s15, s15, 0
	s_branch .Lsc_K_seqdone_t5

.Lsc_K_seqdone_t5:
	s_mov_b32 s17, 81920
	s_waitcnt vmcnt(22)
	s_barrier
	v_add_u32_e32 v140, s17, v3
	v_add_u32_e32 v141, s17, v4
	v_add_u32_e32 v142, s17, v5
	ds_read_b128 v[32:35], v140 offset:0
	ds_read_b128 v[36:39], v141 offset:0
	ds_read_b64_tr_b16 v[64:65], v142 offset:0
	ds_read_b64_tr_b16 v[66:67], v142 offset:128
	ds_read_b64_tr_b16 v[68:69], v142 offset:1024
	ds_read_b64_tr_b16 v[70:71], v142 offset:1152
	ds_read_b128 v[40:43], v140 offset:8192
	ds_read_b128 v[44:47], v141 offset:8192
	ds_read_b64_tr_b16 v[72:73], v142 offset:2048
	ds_read_b64_tr_b16 v[74:75], v142 offset:2176
	ds_read_b64_tr_b16 v[76:77], v142 offset:3072
	ds_read_b64_tr_b16 v[78:79], v142 offset:3200
	ds_read_b128 v[48:51], v140 offset:16384
	ds_read_b128 v[52:55], v141 offset:16384
	ds_read_b64_tr_b16 v[80:81], v142 offset:4096
	ds_read_b64_tr_b16 v[82:83], v142 offset:4224
	ds_read_b64_tr_b16 v[84:85], v142 offset:5120
	ds_read_b64_tr_b16 v[86:87], v142 offset:5248
	ds_read_b128 v[56:59], v140 offset:24576
	ds_read_b128 v[60:63], v141 offset:24576
	ds_read_b64_tr_b16 v[88:89], v142 offset:6144
	ds_read_b64_tr_b16 v[90:91], v142 offset:6272
	ds_read_b64_tr_b16 v[92:93], v142 offset:7168
	ds_read_b64_tr_b16 v[94:95], v142 offset:7296
	s_waitcnt lgkmcnt(12)
	v_mfma_f32_16x16x32_bf16 v[96:99], v[32:35], v[10:13], 0
	v_mfma_f32_16x16x32_bf16 v[112:115], v[64:67], v[32:35], 0
	v_mfma_f32_16x16x32_bf16 v[96:99], v[36:39], v[10:13], v[96:99]
	v_mfma_f32_16x16x32_bf16 v[112:115], v[68:71], v[36:39], v[112:115]
	v_mfma_f32_16x16x32_bf16 v[100:103], v[40:43], v[10:13], 0
	v_mfma_f32_16x16x32_bf16 v[116:119], v[72:75], v[40:43], 0
	v_mfma_f32_16x16x32_bf16 v[100:103], v[44:47], v[10:13], v[100:103]
	v_mfma_f32_16x16x32_bf16 v[116:119], v[76:79], v[44:47], v[116:119]
	s_waitcnt lgkmcnt(6)
	v_mfma_f32_16x16x32_bf16 v[104:107], v[48:51], v[10:13], 0
	v_mfma_f32_16x16x32_bf16 v[120:123], v[80:83], v[48:51], 0
	v_mfma_f32_16x16x32_bf16 v[104:107], v[52:55], v[10:13], v[104:107]
	v_mfma_f32_16x16x32_bf16 v[120:123], v[84:87], v[52:55], v[120:123]
	s_waitcnt lgkmcnt(0)
	v_mfma_f32_16x16x32_bf16 v[108:111], v[56:59], v[10:13], 0
	v_mfma_f32_16x16x32_bf16 v[124:127], v[88:91], v[56:59], 0
	v_mfma_f32_16x16x32_bf16 v[108:111], v[60:63], v[10:13], v[108:111]
	v_mfma_f32_16x16x32_bf16 v[124:127], v[92:95], v[60:63], v[124:127]
	s_cmp_eq_u32 s6, 0
	s_cbranch_scc1 .Lsc_K_zver_t6
	v_cvt_pk_bf16_f32 v152, v16, v17
	v_cvt_pk_bf16_f32 v153, v18, v19
	global_store_dwordx2 v7, v[152:153], s[12:13]
	v_pk_add_f32 v[16:17], v[16:17], v[112:113]
	v_pk_add_f32 v[18:19], v[18:19], v[114:115]
	v_pk_add_f32 v[20:21], v[20:21], v[96:97]
	v_pk_add_f32 v[22:23], v[22:23], v[98:99]
	v_cvt_pk_bf16_f32 v154, v16, v17
	v_cvt_pk_bf16_f32 v155, v18, v19
	global_store_dwordx2 v160, v[154:155], s[12:13]
	v_pk_add_f32 v[16:17], v[16:17], v[116:117]
	v_pk_add_f32 v[18:19], v[18:19], v[118:119]
	v_pk_add_f32 v[20:21], v[20:21], v[100:101]
	v_pk_add_f32 v[22:23], v[22:23], v[102:103]
	v_cvt_pk_bf16_f32 v152, v16, v17
	v_cvt_pk_bf16_f32 v153, v18, v19
	global_store_dwordx2 v161, v[152:153], s[12:13]
	v_pk_add_f32 v[16:17], v[16:17], v[120:121]
	v_pk_add_f32 v[18:19], v[18:19], v[122:123]
	v_pk_add_f32 v[20:21], v[20:21], v[104:105]
	v_pk_add_f32 v[22:23], v[22:23], v[106:107]
	v_cvt_pk_bf16_f32 v154, v16, v17
	v_cvt_pk_bf16_f32 v155, v18, v19
	global_store_dwordx2 v162, v[154:155], s[12:13]
	v_pk_add_f32 v[16:17], v[16:17], v[124:125]
	v_pk_add_f32 v[18:19], v[18:19], v[126:127]
	v_pk_add_f32 v[20:21], v[20:21], v[108:109]
	v_pk_add_f32 v[22:23], v[22:23], v[110:111]
	s_add_u32 s12, s12, 0x20000
	s_addc_u32 s13, s13, 0
	s_add_u32 s14, s14, 0x800
	s_addc_u32 s15, s15, 0
	s_branch .Lsc_K_seqdone_t6

.Lsc_K_seqdone_t6:
	s_mov_b32 s17, 122880
	s_waitcnt vmcnt(12)
	s_barrier
	v_add_u32_e32 v140, s17, v3
	v_add_u32_e32 v141, s17, v4
	v_add_u32_e32 v142, s17, v5
	ds_read_b128 v[32:35], v140 offset:0
	ds_read_b128 v[36:39], v141 offset:0
	ds_read_b64_tr_b16 v[64:65], v142 offset:0
	ds_read_b64_tr_b16 v[66:67], v142 offset:128
	ds_read_b64_tr_b16 v[68:69], v142 offset:1024
	ds_read_b64_tr_b16 v[70:71], v142 offset:1152
	ds_read_b128 v[40:43], v140 offset:8192
	ds_read_b128 v[44:47], v141 offset:8192
	ds_read_b64_tr_b16 v[72:73], v142 offset:2048
	ds_read_b64_tr_b16 v[74:75], v142 offset:2176
	ds_read_b64_tr_b16 v[76:77], v142 offset:3072
	ds_read_b64_tr_b16 v[78:79], v142 offset:3200
	ds_read_b128 v[48:51], v140 offset:16384
	ds_read_b128 v[52:55], v141 offset:16384
	ds_read_b64_tr_b16 v[80:81], v142 offset:4096
	ds_read_b64_tr_b16 v[82:83], v142 offset:4224
	ds_read_b64_tr_b16 v[84:85], v142 offset:5120
	ds_read_b64_tr_b16 v[86:87], v142 offset:5248
	ds_read_b128 v[56:59], v140 offset:24576
	ds_read_b128 v[60:63], v141 offset:24576
	ds_read_b64_tr_b16 v[88:89], v142 offset:6144
	ds_read_b64_tr_b16 v[90:91], v142 offset:6272
	ds_read_b64_tr_b16 v[92:93], v142 offset:7168
	ds_read_b64_tr_b16 v[94:95], v142 offset:7296
	s_waitcnt lgkmcnt(12)
	v_mfma_f32_16x16x32_bf16 v[96:99], v[32:35], v[10:13], 0
	v_mfma_f32_16x16x32_bf16 v[112:115], v[64:67], v[32:35], 0
	v_mfma_f32_16x16x32_bf16 v[96:99], v[36:39], v[10:13], v[96:99]
	v_mfma_f32_16x16x32_bf16 v[112:115], v[68:71], v[36:39], v[112:115]
	v_mfma_f32_16x16x32_bf16 v[100:103], v[40:43], v[10:13], 0
	v_mfma_f32_16x16x32_bf16 v[116:119], v[72:75], v[40:43], 0
	v_mfma_f32_16x16x32_bf16 v[100:103], v[44:47], v[10:13], v[100:103]
	v_mfma_f32_16x16x32_bf16 v[116:119], v[76:79], v[44:47], v[116:119]
	s_waitcnt lgkmcnt(6)
	v_mfma_f32_16x16x32_bf16 v[104:107], v[48:51], v[10:13], 0
	v_mfma_f32_16x16x32_bf16 v[120:123], v[80:83], v[48:51], 0
	v_mfma_f32_16x16x32_bf16 v[104:107], v[52:55], v[10:13], v[104:107]
	v_mfma_f32_16x16x32_bf16 v[120:123], v[84:87], v[52:55], v[120:123]
	s_waitcnt lgkmcnt(0)
	v_mfma_f32_16x16x32_bf16 v[108:111], v[56:59], v[10:13], 0
	v_mfma_f32_16x16x32_bf16 v[124:127], v[88:91], v[56:59], 0
	v_mfma_f32_16x16x32_bf16 v[108:111], v[60:63], v[10:13], v[108:111]
	v_mfma_f32_16x16x32_bf16 v[124:127], v[92:95], v[60:63], v[124:127]
	s_cmp_eq_u32 s6, 0
	s_cbranch_scc1 .Lsc_K_zver_t7
	v_cvt_pk_bf16_f32 v152, v16, v17
	v_cvt_pk_bf16_f32 v153, v18, v19
	global_store_dwordx2 v7, v[152:153], s[12:13]
	v_pk_add_f32 v[16:17], v[16:17], v[112:113]
	v_pk_add_f32 v[18:19], v[18:19], v[114:115]
	v_pk_add_f32 v[20:21], v[20:21], v[96:97]
	v_pk_add_f32 v[22:23], v[22:23], v[98:99]
	v_cvt_pk_bf16_f32 v154, v16, v17
	v_cvt_pk_bf16_f32 v155, v18, v19
	global_store_dwordx2 v160, v[154:155], s[12:13]
	v_pk_add_f32 v[16:17], v[16:17], v[116:117]
	v_pk_add_f32 v[18:19], v[18:19], v[118:119]
	v_pk_add_f32 v[20:21], v[20:21], v[100:101]
	v_pk_add_f32 v[22:23], v[22:23], v[102:103]
	v_cvt_pk_bf16_f32 v152, v16, v17
	v_cvt_pk_bf16_f32 v153, v18, v19
	global_store_dwordx2 v161, v[152:153], s[12:13]
	v_pk_add_f32 v[16:17], v[16:17], v[120:121]
	v_pk_add_f32 v[18:19], v[18:19], v[122:123]
	v_pk_add_f32 v[20:21], v[20:21], v[104:105]
	v_pk_add_f32 v[22:23], v[22:23], v[106:107]
	v_cvt_pk_bf16_f32 v154, v16, v17
	v_cvt_pk_bf16_f32 v155, v18, v19
	global_store_dwordx2 v162, v[154:155], s[12:13]
	v_pk_add_f32 v[16:17], v[16:17], v[124:125]
	v_pk_add_f32 v[18:19], v[18:19], v[126:127]
	v_pk_add_f32 v[20:21], v[20:21], v[108:109]
	v_pk_add_f32 v[22:23], v[22:23], v[110:111]
	s_add_u32 s12, s12, 0x20000
	s_addc_u32 s13, s13, 0
	s_add_u32 s14, s14, 0x800
	s_addc_u32 s15, s15, 0
	s_branch .Lsc_K_seqdone_t7

	.amdhsa_kernel _Z9scan_fastILb1EEvPKtS1_S1_S1_PtS2_Pf
		.amdhsa_group_segment_fixed_size 81920
		.amdhsa_private_segment_fixed_size 0
		.amdhsa_kernarg_size 56
		.amdhsa_user_sgpr_count 2
		.amdhsa_user_sgpr_dispatch_ptr 0
		.amdhsa_user_sgpr_queue_ptr 0
		.amdhsa_user_sgpr_kernarg_segment_ptr 1
		.amdhsa_user_sgpr_dispatch_id 0
		.amdhsa_user_sgpr_kernarg_preload_length 0
		.amdhsa_user_sgpr_kernarg_preload_offset 0
		.amdhsa_user_sgpr_private_segment_size 0
		.amdhsa_uses_dynamic_stack 0
		.amdhsa_enable_private_segment 0
		.amdhsa_system_sgpr_workgroup_id_x 1
		.amdhsa_system_sgpr_workgroup_id_y 0
		.amdhsa_system_sgpr_workgroup_id_z 0
		.amdhsa_system_sgpr_workgroup_info 0
		.amdhsa_system_vgpr_workitem_id 0
		.amdhsa_next_free_vgpr 168
		.amdhsa_next_free_sgpr 56
		.amdhsa_accum_offset 168
		.amdhsa_reserve_vcc 1
		.amdhsa_float_round_mode_32 0
		.amdhsa_float_round_mode_16_64 0
		.amdhsa_float_denorm_mode_32 3
		.amdhsa_float_denorm_mode_16_64 3
		.amdhsa_dx10_clamp 1
		.amdhsa_ieee_mode 1
		.amdhsa_fp16_overflow 0
		.amdhsa_tg_split 0
		.amdhsa_exception_fp_ieee_invalid_op 0
		.amdhsa_exception_fp_denorm_src 0
		.amdhsa_exception_fp_ieee_div_zero 0
		.amdhsa_exception_fp_ieee_overflow 0
		.amdhsa_exception_fp_ieee_underflow 0
		.amdhsa_exception_fp_ieee_inexact 0
		.amdhsa_exception_int_div_zero 0
	.end_amdhsa_kernel

amdhsa.kernels:
  - .agpr_count:     0
    .args:
      - .actual_access:  read_only
        .address_space:  global
        .offset:         0
        .size:           8
        .value_kind:     global_buffer
      - .actual_access:  read_only
        .address_space:  global
        .offset:         8
        .size:           8
        .value_kind:     global_buffer
      - .actual_access:  write_only
        .address_space:  global
        .offset:         16
        .size:           8
        .value_kind:     global_buffer
      - .offset:         24
        .size:           4
        .value_kind:     by_value
      - .offset:         28
        .size:           4
        .value_kind:     by_value
      - .offset:         32
        .size:           4
        .value_kind:     by_value
      - .offset:         36
        .size:           4
        .value_kind:     by_value
    .group_segment_fixed_size: 8256
    .kernarg_segment_align: 8
    .kernarg_segment_size: 40
    .language:       OpenCL C
    .language_version:
      - 2
      - 0
    .max_flat_workgroup_size: 256
    .name:           _Z14gemm_f32_naivePKfS0_Pfiiii
    .private_segment_fixed_size: 0
    .sgpr_count:     24
    .sgpr_spill_count: 0
    .symbol:         _Z14gemm_f32_naivePKfS0_Pfiiii.kd
    .uniform_work_group_size: 1
    .uses_dynamic_stack: false
    .vgpr_count:     76
    .vgpr_spill_count: 0
    .wavefront_size: 64
  - .agpr_count:     0
    .args:
      - .actual_access:  read_only
        .address_space:  global
        .offset:         0
        .size:           8
        .value_kind:     global_buffer
      - .actual_access:  write_only
        .address_space:  global
        .offset:         8
        .size:           8
        .value_kind:     global_buffer
      - .actual_access:  write_only
        .address_space:  global
        .offset:         16
        .size:           8
        .value_kind:     global_buffer
      - .actual_access:  write_only
        .address_space:  global
        .offset:         24
        .size:           8
        .value_kind:     global_buffer
      - .actual_access:  write_only
        .address_space:  global
        .offset:         32
        .size:           8
        .value_kind:     global_buffer
      - .actual_access:  write_only
        .address_space:  global
        .offset:         40
        .size:           8
        .value_kind:     global_buffer
      - .actual_access:  write_only
        .address_space:  global
        .offset:         48
        .size:           8
        .value_kind:     global_buffer
    .group_segment_fixed_size: 0
    .kernarg_segment_align: 8
    .kernarg_segment_size: 56
    .language:       OpenCL C
    .language_version:
      - 2
      - 0
    .max_flat_workgroup_size: 256
    .name:           _Z10post_naivePKfPtS1_S1_S1_S1_S1_
    .private_segment_fixed_size: 0
    .sgpr_count:     28
    .sgpr_spill_count: 0
    .symbol:         _Z10post_naivePKfPtS1_S1_S1_S1_S1_.kd
    .uniform_work_group_size: 1
    .uses_dynamic_stack: false
    .vgpr_count:     38
    .vgpr_spill_count: 0
    .wavefront_size: 64
  - .agpr_count:     0
    .args:
      - .actual_access:  read_only
        .address_space:  global
        .offset:         0
        .size:           8
        .value_kind:     global_buffer
      - .actual_access:  read_only
        .address_space:  global
        .offset:         8
        .size:           8
        .value_kind:     global_buffer
      - .actual_access:  read_only
        .address_space:  global
        .offset:         16
        .size:           8
        .value_kind:     global_buffer
      - .actual_access:  read_only
        .address_space:  global
        .offset:         24
        .size:           8
        .value_kind:     global_buffer
      - .actual_access:  read_only
        .address_space:  global
        .offset:         32
        .size:           8
        .value_kind:     global_buffer
      - .actual_access:  read_only
        .address_space:  global
        .offset:         40
        .size:           8
        .value_kind:     global_buffer
      - .actual_access:  read_only
        .address_space:  global
        .offset:         48
        .size:           8
        .value_kind:     global_buffer
      - .actual_access:  write_only
        .address_space:  global
        .offset:         56
        .size:           8
        .value_kind:     global_buffer
      - .actual_access:  write_only
        .address_space:  global
        .offset:         64
        .size:           8
        .value_kind:     global_buffer
      - .actual_access:  write_only
        .address_space:  global
        .offset:         72
        .size:           8
        .value_kind:     global_buffer
      - .actual_access:  write_only
        .address_space:  global
        .offset:         80
        .size:           8
        .value_kind:     global_buffer
    .group_segment_fixed_size: 1152
    .kernarg_segment_align: 8
    .kernarg_segment_size: 88
    .language:       OpenCL C
    .language_version:
      - 2
      - 0
    .max_flat_workgroup_size: 256
    .name:           _Z11gates_naivePKfS0_S0_S0_S0_S0_S0_PtS1_S1_S1_
    .private_segment_fixed_size: 0
    .sgpr_count:     32
    .sgpr_spill_count: 0
    .symbol:         _Z11gates_naivePKfS0_S0_S0_S0_S0_S0_PtS1_S1_S1_.kd
    .uniform_work_group_size: 1
    .uses_dynamic_stack: false
    .vgpr_count:     66
    .vgpr_spill_count: 0
    .wavefront_size: 64
  - .agpr_count:     0
    .args:
      - .actual_access:  read_only
        .address_space:  global
        .offset:         0
        .size:           8
        .value_kind:     global_buffer
      - .actual_access:  read_only
        .address_space:  global
        .offset:         8
        .size:           8
        .value_kind:     global_buffer
      - .actual_access:  read_only
        .address_space:  global
        .offset:         16
        .size:           8
        .value_kind:     global_buffer
      - .actual_access:  read_only
        .address_space:  global
        .offset:         24
        .size:           8
        .value_kind:     global_buffer
      - .actual_access:  read_only
        .address_space:  global
        .offset:         32
        .size:           8
        .value_kind:     global_buffer
      - .actual_access:  read_only
        .address_space:  global
        .offset:         40
        .size:           8
        .value_kind:     global_buffer
      - .actual_access:  read_only
        .address_space:  global
        .offset:         48
        .size:           8
        .value_kind:     global_buffer
      - .actual_access:  write_only
        .address_space:  global
        .offset:         56
        .size:           8
        .value_kind:     global_buffer
    .group_segment_fixed_size: 12560
    .kernarg_segment_align: 8
    .kernarg_segment_size: 64
    .language:       OpenCL C
    .language_version:
      - 2
      - 0
    .max_flat_workgroup_size: 256
    .name:           _Z10attn_naivePKtS0_S0_S0_S0_S0_PKfPf
    .private_segment_fixed_size: 0
    .sgpr_count:     33
    .sgpr_spill_count: 0
    .symbol:         _Z10attn_naivePKtS0_S0_S0_S0_S0_PKfPf.kd
    .uniform_work_group_size: 1
    .uses_dynamic_stack: false
    .vgpr_count:     82
    .vgpr_spill_count: 0
    .wavefront_size: 64
  - .agpr_count:     0
    .args:
      - .address_space:  global
        .offset:         0
        .size:           8
        .value_kind:     global_buffer
      - .address_space:  global
        .offset:         8
        .size:           8
        .value_kind:     global_buffer
      - .actual_access:  write_only
        .address_space:  global
        .offset:         16
        .size:           8
        .value_kind:     global_buffer
    .group_segment_fixed_size: 0
    .kernarg_segment_align: 8
    .kernarg_segment_size: 24
    .language:       OpenCL C
    .language_version:
      - 2
      - 0
    .max_flat_workgroup_size: 512
    .name:           _Z8gemm_outPKtS0_Pf
    .private_segment_fixed_size: 0
    .sgpr_count:     26
    .sgpr_spill_count: 0
    .symbol:         _Z8gemm_outPKtS0_Pf.kd
    .uniform_work_group_size: 1
    .uses_dynamic_stack: false
    .vgpr_count:     158
    .vgpr_spill_count: 0
    .wavefront_size: 64
  - .agpr_count:     0
    .args:
      - .address_space:  global
        .offset:         0
        .size:           8
        .value_kind:     global_buffer
      - .address_space:  global
        .offset:         8
        .size:           8
        .value_kind:     global_buffer
      - .actual_access:  write_only
        .address_space:  global
        .offset:         16
        .size:           8
        .value_kind:     global_buffer
    .group_segment_fixed_size: 0
    .kernarg_segment_align: 8
    .kernarg_segment_size: 24
    .language:       OpenCL C
    .language_version:
      - 2
      - 0
    .max_flat_workgroup_size: 512
    .name:           _Z9gemm_out2PKtS0_Pf
    .private_segment_fixed_size: 0
    .sgpr_count:     27
    .sgpr_spill_count: 0
    .symbol:         _Z9gemm_out2PKtS0_Pf.kd
    .uniform_work_group_size: 1
    .uses_dynamic_stack: false
    .vgpr_count:     146
    .vgpr_spill_count: 0
    .wavefront_size: 64
  - .agpr_count:     0
    .args:
      - .actual_access:  read_only
        .address_space:  global
        .offset:         0
        .size:           8
        .value_kind:     global_buffer
      - .actual_access:  write_only
        .address_space:  global
        .offset:         8
        .size:           8
        .value_kind:     global_buffer
    .group_segment_fixed_size: 0
    .kernarg_segment_align: 8
    .kernarg_segment_size: 16
    .language:       OpenCL C
    .language_version:
      - 2
      - 0
    .max_flat_workgroup_size: 256
    .name:           _Z6conv_xPKfPt
    .private_segment_fixed_size: 0
    .sgpr_count:     14
    .sgpr_spill_count: 0
    .symbol:         _Z6conv_xPKfPt.kd
    .uniform_work_group_size: 1
    .uses_dynamic_stack: false
    .vgpr_count:     12
    .vgpr_spill_count: 0
    .wavefront_size: 64
  - .agpr_count:     0
    .args:
      - .actual_access:  read_only
        .address_space:  global
        .offset:         0
        .size:           8
        .value_kind:     global_buffer
      - .actual_access:  read_only
        .address_space:  global
        .offset:         8
        .size:           8
        .value_kind:     global_buffer
      - .actual_access:  read_only
        .address_space:  global
        .offset:         16
        .size:           8
        .value_kind:     global_buffer
      - .actual_access:  read_only
        .address_space:  global
        .offset:         24
        .size:           8
        .value_kind:     global_buffer
      - .actual_access:  read_only
        .address_space:  global
        .offset:         32
        .size:           8
        .value_kind:     global_buffer
      - .actual_access:  write_only
        .address_space:  global
        .offset:         40
        .size:           8
        .value_kind:     global_buffer
      - .actual_access:  write_only
        .address_space:  global
        .offset:         48
        .size:           8
        .value_kind:     global_buffer
    .group_segment_fixed_size: 16640
    .kernarg_segment_align: 8
    .kernarg_segment_size: 56
    .language:       OpenCL C
    .language_version:
      - 2
      - 0
    .max_flat_workgroup_size: 256
    .name:           _Z7conv_wTPKfS0_S0_S0_S0_PtS1_
    .private_segment_fixed_size: 0
    .sgpr_count:     26
    .sgpr_spill_count: 0
    .symbol:         _Z7conv_wTPKfS0_S0_S0_S0_PtS1_.kd
    .uniform_work_group_size: 1
    .uses_dynamic_stack: false
    .vgpr_count:     51
    .vgpr_spill_count: 0
    .wavefront_size: 64
  - .agpr_count:     0
    .args:
      - .actual_access:  read_only
        .address_space:  global
        .offset:         0
        .size:           8
        .value_kind:     global_buffer
      - .actual_access:  read_only
        .address_space:  global
        .offset:         8
        .size:           8
        .value_kind:     global_buffer
      - .actual_access:  write_only
        .address_space:  global
        .offset:         16
        .size:           8
        .value_kind:     global_buffer
    .group_segment_fixed_size: 0
    .kernarg_segment_align: 8
    .kernarg_segment_size: 24
    .language:       OpenCL C
    .language_version:
      - 2
      - 0
    .max_flat_workgroup_size: 256
    .name:           _Z7conv_w1PKfS0_Pt
    .private_segment_fixed_size: 0
    .sgpr_count:     16
    .sgpr_spill_count: 0
    .symbol:         _Z7conv_w1PKfS0_Pt.kd
    .uniform_work_group_size: 1
    .uses_dynamic_stack: false
    .vgpr_count:     6
    .vgpr_spill_count: 0
    .wavefront_size: 64
  - .agpr_count:     8
    .args:
      - .actual_access:  read_only
        .address_space:  global
        .offset:         0
        .size:           8
        .value_kind:     global_buffer
      - .actual_access:  read_only
        .address_space:  global
        .offset:         8
        .size:           8
        .value_kind:     global_buffer
      - .actual_access:  read_only
        .address_space:  global
        .offset:         16
        .size:           8
        .value_kind:     global_buffer
      - .actual_access:  read_only
        .address_space:  global
        .offset:         24
        .size:           8
        .value_kind:     global_buffer
      - .actual_access:  read_only
        .address_space:  global
        .offset:         32
        .size:           8
        .value_kind:     global_buffer
      - .actual_access:  read_only
        .address_space:  global
        .offset:         40
        .size:           8
        .value_kind:     global_buffer
      - .actual_access:  write_only
        .address_space:  global
        .offset:         48
        .size:           8
        .value_kind:     global_buffer
      - .actual_access:  write_only
        .address_space:  global
        .offset:         56
        .size:           8
        .value_kind:     global_buffer
      - .actual_access:  write_only
        .address_space:  global
        .offset:         64
        .size:           8
        .value_kind:     global_buffer
    .group_segment_fixed_size: 10240
    .kernarg_segment_align: 8
    .kernarg_segment_size: 72
    .language:       OpenCL C
    .language_version:
      - 2
      - 0
    .max_flat_workgroup_size: 256
    .name:           _Z10gates_fastPKtS0_PKfS2_S2_S2_PtS3_S3_
    .private_segment_fixed_size: 0
    .sgpr_count:     24
    .sgpr_spill_count: 0
    .symbol:         _Z10gates_fastPKtS0_PKfS2_S2_S2_PtS3_S3_.kd
    .uniform_work_group_size: 1
    .uses_dynamic_stack: false
    .vgpr_count:     96
    .vgpr_spill_count: 0
    .wavefront_size: 64
  - .agpr_count:     4
    .args:
      - .actual_access:  read_only
        .address_space:  global
        .offset:         0
        .size:           8
        .value_kind:     global_buffer
      - .actual_access:  read_only
        .address_space:  global
        .offset:         8
        .size:           8
        .value_kind:     global_buffer
      - .actual_access:  read_only
        .address_space:  global
        .offset:         16
        .size:           8
        .value_kind:     global_buffer
      - .actual_access:  read_only
        .address_space:  global
        .offset:         24
        .size:           8
        .value_kind:     global_buffer
      - .actual_access:  write_only
        .address_space:  global
        .offset:         32
        .size:           8
        .value_kind:     global_buffer
      - .actual_access:  write_only
        .address_space:  global
        .offset:         40
        .size:           8
        .value_kind:     global_buffer
      - .actual_access:  write_only
        .address_space:  global
        .offset:         48
        .size:           8
        .value_kind:     global_buffer
    .group_segment_fixed_size: 0
    .kernarg_segment_align: 8
    .kernarg_segment_size: 56
    .language:       OpenCL C
    .language_version:
      - 2
      - 0
    .max_flat_workgroup_size: 256
    .name:           _Z10state_fastPKtS0_S0_S0_PtS1_Pf
    .private_segment_fixed_size: 0
    .sgpr_count:     20
    .sgpr_spill_count: 0
    .symbol:         _Z10state_fastPKtS0_S0_S0_PtS1_Pf.kd
    .uniform_work_group_size: 1
    .uses_dynamic_stack: false
    .vgpr_count:     184
    .vgpr_spill_count: 0
    .wavefront_size: 64
  - .agpr_count:     0
    .args:
      - .actual_access:  read_only
        .address_space:  global
        .offset:         0
        .size:           8
        .value_kind:     global_buffer
      - .actual_access:  read_only
        .address_space:  global
        .offset:         8
        .size:           8
        .value_kind:     global_buffer
      - .actual_access:  read_only
        .address_space:  global
        .offset:         16
        .size:           8
        .value_kind:     global_buffer
      - .actual_access:  write_only
        .address_space:  global
        .offset:         24
        .size:           8
        .value_kind:     global_buffer
      - .actual_access:  write_only
        .address_space:  global
        .offset:         32
        .size:           8
        .value_kind:     global_buffer
      - .actual_access:  write_only
        .address_space:  global
        .offset:         40
        .size:           8
        .value_kind:     global_buffer
    .group_segment_fixed_size: 0
    .kernarg_segment_align: 8
    .kernarg_segment_size: 48
    .language:       OpenCL C
    .language_version:
      - 2
      - 0
    .max_flat_workgroup_size: 256
    .name:           _Z11prefix_fastPKtS0_PKfPtS3_Pf
    .private_segment_fixed_size: 0
    .sgpr_count:     106
    .sgpr_spill_count: 41
    .symbol:         _Z11prefix_fastPKtS0_PKfPtS3_Pf.kd
    .uniform_work_group_size: 1
    .uses_dynamic_stack: false
    .vgpr_count:     205
    .vgpr_spill_count: 0
    .wavefront_size: 64
  - .agpr_count:     0
    .args:
      - .address_space:  global
        .offset:         0
        .size:           8
        .value_kind:     global_buffer
      - .address_space:  global
        .offset:         8
        .size:           8
        .value_kind:     global_buffer
      - .address_space:  global
        .offset:         16
        .size:           8
        .value_kind:     global_buffer
      - .actual_access:  read_only
        .address_space:  global
        .offset:         24
        .size:           8
        .value_kind:     global_buffer
      - .address_space:  global
        .offset:         32
        .size:           8
        .value_kind:     global_buffer
      - .address_space:  global
        .offset:         40
        .size:           8
        .value_kind:     global_buffer
      - .address_space:  global
        .offset:         48
        .size:           8
        .value_kind:     global_buffer
      - .address_space:  global
        .offset:         56
        .size:           8
        .value_kind:     global_buffer
      - .address_space:  global
        .offset:         64
        .size:           8
        .value_kind:     global_buffer
      - .address_space:  global
        .offset:         72
        .size:           8
        .value_kind:     global_buffer
      - .address_space:  global
        .offset:         80
        .size:           8
        .value_kind:     global_buffer
      - .actual_access:  write_only
        .address_space:  global
        .offset:         88
        .size:           8
        .value_kind:     global_buffer
    .group_segment_fixed_size: 0
    .kernarg_segment_align: 8
    .kernarg_segment_size: 96
    .language:       OpenCL C
    .language_version:
      - 2
      - 0
    .max_flat_workgroup_size: 512
    .name:           _Z9attn_fastPKtS0_S0_S0_S0_S0_S0_S0_S0_PKfS2_Pt
    .private_segment_fixed_size: 0
    .sgpr_count:     50
    .sgpr_spill_count: 0
    .symbol:         _Z9attn_fastPKtS0_S0_S0_S0_S0_S0_S0_S0_PKfS2_Pt.kd
    .uniform_work_group_size: 1
    .uses_dynamic_stack: false
    .vgpr_count:     152
    .vgpr_spill_count: 0
    .wavefront_size: 64
  - .agpr_count:     12
    .args:
      - .actual_access:  read_only
        .address_space:  global
        .offset:         0
        .size:           8
        .value_kind:     global_buffer
      - .actual_access:  read_only
        .address_space:  global
        .offset:         8
        .size:           8
        .value_kind:     global_buffer
      - .actual_access:  read_only
        .address_space:  global
        .offset:         16
        .size:           8
        .value_kind:     global_buffer
      - .actual_access:  read_only
        .address_space:  global
        .offset:         24
        .size:           8
        .value_kind:     global_buffer
      - .actual_access:  read_only
        .address_space:  global
        .offset:         32
        .size:           8
        .value_kind:     global_buffer
      - .actual_access:  read_only
        .address_space:  global
        .offset:         40
        .size:           8
        .value_kind:     global_buffer
      - .actual_access:  read_only
        .address_space:  global
        .offset:         48
        .size:           8
        .value_kind:     global_buffer
      - .actual_access:  read_only
        .address_space:  global
        .offset:         56
        .size:           8
        .value_kind:     global_buffer
      - .actual_access:  read_only
        .address_space:  global
        .offset:         64
        .size:           8
        .value_kind:     global_buffer
      - .actual_access:  read_only
        .address_space:  global
        .offset:         72
        .size:           8
        .value_kind:     global_buffer
      - .actual_access:  read_only
        .address_space:  global
        .offset:         80
        .size:           8
        .value_kind:     global_buffer
      - .actual_access:  read_only
        .address_space:  global
        .offset:         88
        .size:           8
        .value_kind:     global_buffer
      - .actual_access:  write_only
        .address_space:  global
        .offset:         96
        .size:           8
        .value_kind:     global_buffer
      - .actual_access:  write_only
        .address_space:  global
        .offset:         104
        .size:           8
        .value_kind:     global_buffer
      - .actual_access:  write_only
        .address_space:  global
        .offset:         112
        .size:           8
        .value_kind:     global_buffer
      - .actual_access:  write_only
        .address_space:  global
        .offset:         120
        .size:           8
        .value_kind:     global_buffer
      - .actual_access:  write_only
        .address_space:  global
        .offset:         128
        .size:           8
        .value_kind:     global_buffer
      - .actual_access:  write_only
        .address_space:  global
        .offset:         136
        .size:           8
        .value_kind:     global_buffer
    .group_segment_fixed_size: 16640
    .kernarg_segment_align: 8
    .kernarg_segment_size: 144
    .language:       OpenCL C
    .language_version:
      - 2
      - 0
    .max_flat_workgroup_size: 256
    .name:           _Z11prep_kernelPKfS0_S0_S0_S0_S0_S0_S0_S0_S0_S0_S0_PtS1_S1_S1_S1_S1_
    .private_segment_fixed_size: 0
    .sgpr_count:     34
    .sgpr_spill_count: 0
    .symbol:         _Z11prep_kernelPKfS0_S0_S0_S0_S0_S0_S0_S0_S0_S0_S0_PtS1_S1_S1_S1_S1_.kd
    .uniform_work_group_size: 1
    .uses_dynamic_stack: false
    .vgpr_count:     124
    .vgpr_spill_count: 0
    .wavefront_size: 64
  - .agpr_count:     0
    .args:
      - .address_space:  global
        .offset:         0
        .size:           8
        .value_kind:     global_buffer
      - .address_space:  global
        .offset:         8
        .size:           8
        .value_kind:     global_buffer
      - .offset:         16
        .size:           4
        .value_kind:     by_value
      - .offset:         20
        .size:           4
        .value_kind:     by_value
      - .offset:         24
        .size:           4
        .value_kind:     by_value
      - .offset:         28
        .size:           4
        .value_kind:     by_value
      - .address_space:  global
        .offset:         32
        .size:           8
        .value_kind:     global_buffer
    .group_segment_fixed_size: 0
    .kernarg_segment_align: 8
    .kernarg_segment_size: 40
    .language:       OpenCL C
    .language_version:
      - 2
      - 0
    .max_flat_workgroup_size: 1024
    .name:           _Z9dbg_cmp16PKtS0_iiffPf
    .private_segment_fixed_size: 0
    .sgpr_count:     18
    .sgpr_spill_count: 0
    .symbol:         _Z9dbg_cmp16PKtS0_iiffPf.kd
    .uniform_work_group_size: 1
    .uses_dynamic_stack: false
    .vgpr_count:     5
    .vgpr_spill_count: 0
    .wavefront_size: 64
  - .agpr_count:     0
    .args:
      - .address_space:  global
        .offset:         0
        .size:           8
        .value_kind:     global_buffer
      - .address_space:  global
        .offset:         8
        .size:           8
        .value_kind:     global_buffer
      - .offset:         16
        .size:           4
        .value_kind:     by_value
      - .offset:         20
        .size:           4
        .value_kind:     by_value
      - .offset:         24
        .size:           56
        .value_kind:     by_value
    .group_segment_fixed_size: 0
    .kernarg_segment_align: 8
    .kernarg_segment_size: 80
    .language:       OpenCL C
    .language_version:
      - 2
      - 0
    .max_flat_workgroup_size: 512
    .name:           _Z5gemm8ILi0EEvPKtS1_ii7EpiArgs
    .private_segment_fixed_size: 0
    .sgpr_count:     36
    .sgpr_spill_count: 0
    .symbol:         _Z5gemm8ILi0EEvPKtS1_ii7EpiArgs.kd
    .uniform_work_group_size: 1
    .uses_dynamic_stack: false
    .vgpr_count:     246
    .vgpr_spill_count: 0
    .wavefront_size: 64
  - .agpr_count:     0
    .args:
      - .address_space:  global
        .offset:         0
        .size:           8
        .value_kind:     global_buffer
      - .address_space:  global
        .offset:         8
        .size:           8
        .value_kind:     global_buffer
      - .address_space:  global
        .offset:         16
        .size:           8
        .value_kind:     global_buffer
      - .address_space:  global
        .offset:         24
        .size:           8
        .value_kind:     global_buffer
      - .actual_access:  write_only
        .address_space:  global
        .offset:         32
        .size:           8
        .value_kind:     global_buffer
      - .actual_access:  write_only
        .address_space:  global
        .offset:         40
        .size:           8
        .value_kind:     global_buffer
      - .actual_access:  write_only
        .address_space:  global
        .offset:         48
        .size:           8
        .value_kind:     global_buffer
    .group_segment_fixed_size: 81920
    .kernarg_segment_align: 8
    .kernarg_segment_size: 56
    .language:       OpenCL C
    .language_version:
      - 2
      - 0
    .max_flat_workgroup_size: 256
    .name:           _Z9scan_fastILb1EEvPKtS1_S1_S1_PtS2_Pf
    .private_segment_fixed_size: 0
    .sgpr_count:     62
    .sgpr_spill_count: 0
    .symbol:         _Z9scan_fastILb1EEvPKtS1_S1_S1_PtS2_Pf.kd
    .uniform_work_group_size: 1
    .uses_dynamic_stack: false
    .vgpr_count:     168
    .vgpr_spill_count: 0
    .wavefront_size: 64
